# conv phase: the 30 guarded input rows loaded up front (clamped row index) instead of one round trip per row
# baseline (speedup 1.0000x reference)
.LBB0_267:
	v_add_u32_e32 v80, 30, v144
	v_and_b32_e32 v44, 0xff8, v80
	s_waitcnt vmcnt(3)
	v_mov_b64_e32 v[42:43], v[2:3]
	v_max_i32_e32 v252, 0, v144
	v_mad_i64_i32 v[250:251], s[24:25], v252, s27, v[78:79]
	global_load_dwordx2 v[96:97], v[250:251], off
	global_load_dwordx2 v[98:99], v[250:251], off offset:512
	v_add_u32_e32 v252, 1, v144
	v_max_i32_e32 v252, 0, v252
	v_mad_i64_i32 v[250:251], s[24:25], v252, s27, v[78:79]
	global_load_dwordx2 v[100:101], v[250:251], off
	global_load_dwordx2 v[102:103], v[250:251], off offset:512
	v_add_u32_e32 v252, 2, v144
	v_max_i32_e32 v252, 0, v252
	v_mad_i64_i32 v[250:251], s[24:25], v252, s27, v[78:79]
	global_load_dwordx2 v[104:105], v[250:251], off
	global_load_dwordx2 v[106:107], v[250:251], off offset:512
	v_add_u32_e32 v252, 3, v144
	v_max_i32_e32 v252, 0, v252
	v_mad_i64_i32 v[250:251], s[24:25], v252, s27, v[78:79]
	global_load_dwordx2 v[108:109], v[250:251], off
	global_load_dwordx2 v[110:111], v[250:251], off offset:512
	v_add_u32_e32 v252, 4, v144
	v_max_i32_e32 v252, 0, v252
	v_mad_i64_i32 v[250:251], s[24:25], v252, s27, v[78:79]
	global_load_dwordx2 v[112:113], v[250:251], off
	global_load_dwordx2 v[114:115], v[250:251], off offset:512
	v_add_u32_e32 v252, 5, v144
	v_max_i32_e32 v252, 0, v252
	v_mad_i64_i32 v[250:251], s[24:25], v252, s27, v[78:79]
	global_load_dwordx2 v[116:117], v[250:251], off
	global_load_dwordx2 v[118:119], v[250:251], off offset:512
	v_add_u32_e32 v252, 6, v144
	v_max_i32_e32 v252, 0, v252
	v_mad_i64_i32 v[250:251], s[24:25], v252, s27, v[78:79]
	global_load_dwordx2 v[120:121], v[250:251], off
	global_load_dwordx2 v[122:123], v[250:251], off offset:512
	v_add_u32_e32 v252, 7, v144
	v_max_i32_e32 v252, 0, v252
	v_mad_i64_i32 v[250:251], s[24:25], v252, s27, v[78:79]
	global_load_dwordx2 v[124:125], v[250:251], off
	global_load_dwordx2 v[126:127], v[250:251], off offset:512
	v_add_u32_e32 v252, 8, v144
	v_max_i32_e32 v252, 0, v252
	v_mad_i64_i32 v[250:251], s[24:25], v252, s27, v[78:79]
	global_load_dwordx2 v[128:129], v[250:251], off
	global_load_dwordx2 v[130:131], v[250:251], off offset:512
	v_add_u32_e32 v252, 9, v144
	v_max_i32_e32 v252, 0, v252
	v_mad_i64_i32 v[250:251], s[24:25], v252, s27, v[78:79]
	global_load_dwordx2 v[132:133], v[250:251], off
	global_load_dwordx2 v[134:135], v[250:251], off offset:512
	v_add_u32_e32 v252, 10, v144
	v_max_i32_e32 v252, 0, v252
	v_mad_i64_i32 v[250:251], s[24:25], v252, s27, v[78:79]
	global_load_dwordx2 v[136:137], v[250:251], off
	global_load_dwordx2 v[138:139], v[250:251], off offset:512
	v_add_u32_e32 v252, 11, v144
	v_max_i32_e32 v252, 0, v252
	v_mad_i64_i32 v[250:251], s[24:25], v252, s27, v[78:79]
	global_load_dwordx2 v[140:141], v[250:251], off
	global_load_dwordx2 v[142:143], v[250:251], off offset:512
	v_add_u32_e32 v252, 12, v144
	v_max_i32_e32 v252, 0, v252
	v_mad_i64_i32 v[250:251], s[24:25], v252, s27, v[78:79]
	global_load_dwordx2 v[152:153], v[250:251], off
	global_load_dwordx2 v[154:155], v[250:251], off offset:512
	v_add_u32_e32 v252, 13, v144
	v_max_i32_e32 v252, 0, v252
	v_mad_i64_i32 v[250:251], s[24:25], v252, s27, v[78:79]
	global_load_dwordx2 v[156:157], v[250:251], off
	global_load_dwordx2 v[158:159], v[250:251], off offset:512
	v_add_u32_e32 v252, 14, v144
	v_max_i32_e32 v252, 0, v252
	v_mad_i64_i32 v[250:251], s[24:25], v252, s27, v[78:79]
	global_load_dwordx2 v[162:163], v[250:251], off
	global_load_dwordx2 v[164:165], v[250:251], off offset:512
	v_add_u32_e32 v252, 15, v144
	v_max_i32_e32 v252, 0, v252
	v_mad_i64_i32 v[250:251], s[24:25], v252, s27, v[78:79]
	global_load_dwordx2 v[166:167], v[250:251], off
	global_load_dwordx2 v[168:169], v[250:251], off offset:512
	v_add_u32_e32 v252, 16, v144
	v_max_i32_e32 v252, 0, v252
	v_mad_i64_i32 v[250:251], s[24:25], v252, s27, v[78:79]
	global_load_dwordx2 v[170:171], v[250:251], off
	global_load_dwordx2 v[172:173], v[250:251], off offset:512
	v_add_u32_e32 v252, 17, v144
	v_max_i32_e32 v252, 0, v252
	v_mad_i64_i32 v[250:251], s[24:25], v252, s27, v[78:79]
	global_load_dwordx2 v[176:177], v[250:251], off
	global_load_dwordx2 v[178:179], v[250:251], off offset:512
	v_add_u32_e32 v252, 18, v144
	v_max_i32_e32 v252, 0, v252
	v_mad_i64_i32 v[250:251], s[24:25], v252, s27, v[78:79]
	global_load_dwordx2 v[180:181], v[250:251], off
	global_load_dwordx2 v[182:183], v[250:251], off offset:512
	v_add_u32_e32 v252, 19, v144
	v_max_i32_e32 v252, 0, v252
	v_mad_i64_i32 v[250:251], s[24:25], v252, s27, v[78:79]
	global_load_dwordx2 v[186:187], v[250:251], off
	global_load_dwordx2 v[188:189], v[250:251], off offset:512
	v_add_u32_e32 v252, 20, v144
	v_max_i32_e32 v252, 0, v252
	v_mad_i64_i32 v[250:251], s[24:25], v252, s27, v[78:79]
	global_load_dwordx2 v[206:207], v[250:251], off
	global_load_dwordx2 v[208:209], v[250:251], off offset:512
	v_add_u32_e32 v252, 21, v144
	v_max_i32_e32 v252, 0, v252
	v_mad_i64_i32 v[250:251], s[24:25], v252, s27, v[78:79]
	global_load_dwordx2 v[210:211], v[250:251], off
	global_load_dwordx2 v[212:213], v[250:251], off offset:512
	v_add_u32_e32 v252, 22, v144
	v_max_i32_e32 v252, 0, v252
	v_mad_i64_i32 v[250:251], s[24:25], v252, s27, v[78:79]
	global_load_dwordx2 v[214:215], v[250:251], off
	global_load_dwordx2 v[216:217], v[250:251], off offset:512
	v_add_u32_e32 v252, 23, v144
	v_max_i32_e32 v252, 0, v252
	v_mad_i64_i32 v[250:251], s[24:25], v252, s27, v[78:79]
	global_load_dwordx2 v[218:219], v[250:251], off
	global_load_dwordx2 v[220:221], v[250:251], off offset:512
	v_add_u32_e32 v252, 24, v144
	v_max_i32_e32 v252, 0, v252
	v_mad_i64_i32 v[250:251], s[24:25], v252, s27, v[78:79]
	global_load_dwordx2 v[222:223], v[250:251], off
	global_load_dwordx2 v[224:225], v[250:251], off offset:512
	v_add_u32_e32 v252, 25, v144
	v_max_i32_e32 v252, 0, v252
	v_mad_i64_i32 v[250:251], s[24:25], v252, s27, v[78:79]
	global_load_dwordx2 v[226:227], v[250:251], off
	global_load_dwordx2 v[228:229], v[250:251], off offset:512
	v_add_u32_e32 v252, 26, v144
	v_max_i32_e32 v252, 0, v252
	v_mad_i64_i32 v[250:251], s[24:25], v252, s27, v[78:79]
	global_load_dwordx2 v[230:231], v[250:251], off
	global_load_dwordx2 v[232:233], v[250:251], off offset:512
	v_add_u32_e32 v252, 27, v144
	v_max_i32_e32 v252, 0, v252
	v_mad_i64_i32 v[250:251], s[24:25], v252, s27, v[78:79]
	global_load_dwordx2 v[234:235], v[250:251], off
	global_load_dwordx2 v[236:237], v[250:251], off offset:512
	v_cmp_lt_u32_e32 vcc, 29, v44
	v_mov_b64_e32 v[40:41], v[0:1]
	s_and_saveexec_b64 s[6:7], vcc
	s_cbranch_execz .LBB0_269
	s_waitcnt vmcnt(54)
	v_mov_b64_e32 v[22:23], v[96:97]
	v_mov_b64_e32 v[20:21], v[98:99]
	ds_read_b128 v[16:19], v161 offset:4096
	v_and_b32_e32 v26, 0xffff0000, v21
	v_and_b32_e32 v25, 0xffff0000, v23
	v_lshlrev_b32_e32 v21, 16, v21
	v_lshlrev_b32_e32 v24, 16, v23
	v_and_b32_e32 v23, 0xffff0000, v20
	v_lshlrev_b32_e32 v20, 16, v20
	v_mul_f32_e32 v26, 0xbfb8aa3b, v26
	v_mul_f32_e32 v21, 0xbfb8aa3b, v21
	v_mul_f32_e32 v23, 0xbfb8aa3b, v23
	v_mul_f32_e32 v20, 0xbfb8aa3b, v20
	v_exp_f32_e32 v26, v26
	v_exp_f32_e32 v21, v21
	v_exp_f32_e32 v23, v23
	v_exp_f32_e32 v20, v20
	v_add_f32_e32 v26, 1.0, v26
	v_add_f32_e32 v28, 1.0, v21
	v_add_f32_e32 v23, 1.0, v23
	v_add_f32_e32 v20, 1.0, v20
	v_rcp_f32_e32 v21, v26
	v_rcp_f32_e32 v27, v23
	v_rcp_f32_e32 v26, v20
	v_rcp_f32_e32 v20, v28
	v_and_b32_e32 v23, 0xffff0000, v22
	v_lshlrev_b32_e32 v22, 16, v22
	v_pk_mul_f32 v[22:23], v[26:27], v[22:23]
	v_pk_mul_f32 v[20:21], v[20:21], v[24:25]
	s_waitcnt lgkmcnt(0)
	v_pk_fma_f32 v[40:41], v[16:17], v[22:23], v[0:1]
	v_pk_fma_f32 v[42:43], v[18:19], v[20:21], v[2:3]
.LBB0_269:
	s_or_b64 exec, exec, s[6:7]
	v_add_u32_e32 v252, 28, v144
	v_max_i32_e32 v252, 0, v252
	v_mad_i64_i32 v[250:251], s[24:25], v252, s27, v[78:79]
	global_load_dwordx2 v[238:239], v[250:251], off
	global_load_dwordx2 v[240:241], v[250:251], off offset:512
	v_add_u32_e32 v252, 29, v144
	v_max_i32_e32 v252, 0, v252
	v_mad_i64_i32 v[250:251], s[24:25], v252, s27, v[78:79]
	global_load_dwordx2 v[242:243], v[250:251], off
	global_load_dwordx2 v[244:245], v[250:251], off offset:512
	v_mov_b64_e32 v[38:39], v[2:3]
	v_cmp_lt_u32_e32 vcc, 28, v44
	v_mov_b64_e32 v[36:37], v[0:1]
	s_and_saveexec_b64 s[6:7], vcc
	s_cbranch_execz .LBB0_271
	s_waitcnt vmcnt(56)
	v_mov_b64_e32 v[24:25], v[100:101]
	v_mov_b64_e32 v[26:27], v[102:103]
	ds_read_b128 v[16:19], v161 offset:5120
	ds_read_b128 v[20:23], v161 offset:4096
	v_lshlrev_b32_e32 v28, 16, v24
	v_lshlrev_b32_e32 v30, 16, v26
	v_and_b32_e32 v29, 0xffff0000, v24
	v_and_b32_e32 v24, 0xffff0000, v26
	v_lshlrev_b32_e32 v26, 16, v27
	v_and_b32_e32 v27, 0xffff0000, v27
	v_mul_f32_e32 v30, 0xbfb8aa3b, v30
	v_mul_f32_e32 v24, 0xbfb8aa3b, v24
	v_mul_f32_e32 v26, 0xbfb8aa3b, v26
	v_mul_f32_e32 v27, 0xbfb8aa3b, v27
	v_exp_f32_e32 v30, v30
	v_exp_f32_e32 v24, v24
	v_exp_f32_e32 v26, v26
	v_exp_f32_e32 v27, v27
	v_add_f32_e32 v30, 1.0, v30
	v_add_f32_e32 v24, 1.0, v24
	v_add_f32_e32 v31, 1.0, v26
	v_add_f32_e32 v32, 1.0, v27
	v_rcp_f32_e32 v26, v30
	v_rcp_f32_e32 v27, v24
	v_rcp_f32_e32 v30, v31
	v_rcp_f32_e32 v31, v32
	v_lshlrev_b32_e32 v24, 16, v25
	v_and_b32_e32 v25, 0xffff0000, v25
	v_pk_mul_f32 v[26:27], v[26:27], v[28:29]
	v_pk_mul_f32 v[24:25], v[30:31], v[24:25]
	s_waitcnt lgkmcnt(1)
	v_pk_fma_f32 v[40:41], v[16:17], v[26:27], v[40:41]
	v_pk_fma_f32 v[42:43], v[18:19], v[24:25], v[42:43]
	s_waitcnt lgkmcnt(0)
	v_pk_fma_f32 v[38:39], v[22:23], v[24:25], v[2:3]
	v_pk_fma_f32 v[36:37], v[20:21], v[26:27], v[0:1]
.LBB0_271:
	s_or_b64 exec, exec, s[6:7]
	v_mov_b64_e32 v[34:35], v[2:3]
	v_cmp_lt_u32_e32 vcc, 27, v44
	v_mov_b64_e32 v[32:33], v[0:1]
	s_and_saveexec_b64 s[6:7], vcc
	s_cbranch_execz .LBB0_273
	s_waitcnt vmcnt(54)
	v_mov_b64_e32 v[28:29], v[104:105]
	v_mov_b64_e32 v[30:31], v[106:107]
	ds_read_b128 v[16:19], v161 offset:6144
	ds_read_b128 v[20:23], v161 offset:5120
	ds_read_b128 v[24:27], v161 offset:4096
	v_lshlrev_b32_e32 v32, 16, v28
	v_lshlrev_b32_e32 v34, 16, v30
	v_and_b32_e32 v33, 0xffff0000, v28
	v_and_b32_e32 v28, 0xffff0000, v30
	v_lshlrev_b32_e32 v30, 16, v31
	v_and_b32_e32 v31, 0xffff0000, v31
	v_mul_f32_e32 v34, 0xbfb8aa3b, v34
	v_mul_f32_e32 v28, 0xbfb8aa3b, v28
	v_mul_f32_e32 v30, 0xbfb8aa3b, v30
	v_mul_f32_e32 v31, 0xbfb8aa3b, v31
	v_exp_f32_e32 v34, v34
	v_exp_f32_e32 v28, v28
	v_exp_f32_e32 v30, v30
	v_exp_f32_e32 v31, v31
	v_add_f32_e32 v34, 1.0, v34
	v_add_f32_e32 v28, 1.0, v28
	v_add_f32_e32 v35, 1.0, v30
	v_add_f32_e32 v45, 1.0, v31
	v_rcp_f32_e32 v30, v34
	v_rcp_f32_e32 v31, v28
	v_rcp_f32_e32 v34, v35
	v_rcp_f32_e32 v35, v45
	v_lshlrev_b32_e32 v28, 16, v29
	v_and_b32_e32 v29, 0xffff0000, v29
	v_pk_mul_f32 v[30:31], v[30:31], v[32:33]
	v_pk_mul_f32 v[28:29], v[34:35], v[28:29]
	s_waitcnt lgkmcnt(2)
	v_pk_fma_f32 v[40:41], v[16:17], v[30:31], v[40:41]
	v_pk_fma_f32 v[42:43], v[18:19], v[28:29], v[42:43]
	s_waitcnt lgkmcnt(1)
	v_pk_fma_f32 v[38:39], v[22:23], v[28:29], v[38:39]
	v_pk_fma_f32 v[36:37], v[20:21], v[30:31], v[36:37]
	s_waitcnt lgkmcnt(0)
	v_pk_fma_f32 v[34:35], v[26:27], v[28:29], v[2:3]
	v_pk_fma_f32 v[32:33], v[24:25], v[30:31], v[0:1]
.LBB0_273:
	s_or_b64 exec, exec, s[6:7]
	v_mov_b64_e32 v[22:23], v[2:3]
	v_cmp_lt_u32_e32 vcc, 26, v44
	v_mov_b64_e32 v[20:21], v[0:1]
	s_and_saveexec_b64 s[6:7], vcc
	s_cbranch_execz .LBB0_275
	s_waitcnt vmcnt(52)
	v_mov_b64_e32 v[46:47], v[108:109]
	v_mov_b64_e32 v[48:49], v[110:111]
	ds_read_b128 v[16:19], v161 offset:7168
	ds_read_b128 v[20:23], v161 offset:6144
	ds_read_b128 v[24:27], v161 offset:5120
	ds_read_b128 v[28:31], v161 offset:4096
	v_lshlrev_b32_e32 v50, 16, v46
	v_lshlrev_b32_e32 v45, 16, v48
	v_and_b32_e32 v51, 0xffff0000, v46
	v_and_b32_e32 v46, 0xffff0000, v48
	v_lshlrev_b32_e32 v48, 16, v49
	v_and_b32_e32 v49, 0xffff0000, v49
	v_mul_f32_e32 v45, 0xbfb8aa3b, v45
	v_mul_f32_e32 v46, 0xbfb8aa3b, v46
	v_mul_f32_e32 v48, 0xbfb8aa3b, v48
	v_mul_f32_e32 v49, 0xbfb8aa3b, v49
	v_exp_f32_e32 v45, v45
	v_exp_f32_e32 v46, v46
	v_exp_f32_e32 v48, v48
	v_exp_f32_e32 v49, v49
	v_add_f32_e32 v45, 1.0, v45
	v_add_f32_e32 v46, 1.0, v46
	v_add_f32_e32 v52, 1.0, v48
	v_add_f32_e32 v53, 1.0, v49
	v_rcp_f32_e32 v48, v45
	v_rcp_f32_e32 v49, v46
	v_rcp_f32_e32 v52, v52
	v_rcp_f32_e32 v53, v53
	v_lshlrev_b32_e32 v46, 16, v47
	v_and_b32_e32 v47, 0xffff0000, v47
	v_pk_mul_f32 v[48:49], v[48:49], v[50:51]
	v_pk_mul_f32 v[46:47], v[52:53], v[46:47]
	s_waitcnt lgkmcnt(3)
	v_pk_fma_f32 v[40:41], v[16:17], v[48:49], v[40:41]
	v_pk_fma_f32 v[42:43], v[18:19], v[46:47], v[42:43]
	s_waitcnt lgkmcnt(2)
	v_pk_fma_f32 v[38:39], v[22:23], v[46:47], v[38:39]
	v_pk_fma_f32 v[36:37], v[20:21], v[48:49], v[36:37]
	s_waitcnt lgkmcnt(1)
	v_pk_fma_f32 v[34:35], v[26:27], v[46:47], v[34:35]
	v_pk_fma_f32 v[32:33], v[24:25], v[48:49], v[32:33]
	s_waitcnt lgkmcnt(0)
	v_pk_fma_f32 v[22:23], v[30:31], v[46:47], v[2:3]
	v_pk_fma_f32 v[20:21], v[28:29], v[48:49], v[0:1]
.LBB0_275:
	s_or_b64 exec, exec, s[6:7]
	v_cmp_lt_u32_e32 vcc, 25, v44
	v_mov_b32_e32 v82, v0
	v_mov_b32_e32 v83, v1
	v_mov_b32_e32 v84, v2
	v_mov_b32_e32 v85, v3
	s_and_saveexec_b64 s[6:7], vcc
	s_cbranch_execz .LBB0_277
	s_waitcnt vmcnt(50)
	v_mov_b64_e32 v[54:55], v[112:113]
	v_mov_b64_e32 v[56:57], v[114:115]
	ds_read_b128 v[16:19], v161 offset:8192
	ds_read_b128 v[24:27], v161 offset:7168
	ds_read_b128 v[28:31], v161 offset:6144
	ds_read_b128 v[46:49], v161 offset:5120
	ds_read_b128 v[50:53], v161 offset:4096
	v_lshlrev_b32_e32 v58, 16, v54
	v_lshlrev_b32_e32 v45, 16, v56
	v_and_b32_e32 v59, 0xffff0000, v54
	v_and_b32_e32 v54, 0xffff0000, v56
	v_lshlrev_b32_e32 v56, 16, v57
	v_and_b32_e32 v57, 0xffff0000, v57
	v_mul_f32_e32 v45, 0xbfb8aa3b, v45
	v_mul_f32_e32 v54, 0xbfb8aa3b, v54
	v_mul_f32_e32 v56, 0xbfb8aa3b, v56
	v_mul_f32_e32 v57, 0xbfb8aa3b, v57
	v_exp_f32_e32 v45, v45
	v_exp_f32_e32 v54, v54
	v_exp_f32_e32 v56, v56
	v_exp_f32_e32 v57, v57
	v_add_f32_e32 v45, 1.0, v45
	v_add_f32_e32 v54, 1.0, v54
	v_add_f32_e32 v60, 1.0, v56
	v_add_f32_e32 v61, 1.0, v57
	v_rcp_f32_e32 v56, v45
	v_rcp_f32_e32 v57, v54
	v_rcp_f32_e32 v60, v60
	v_rcp_f32_e32 v61, v61
	v_lshlrev_b32_e32 v54, 16, v55
	v_and_b32_e32 v55, 0xffff0000, v55
	v_pk_mul_f32 v[56:57], v[56:57], v[58:59]
	v_pk_mul_f32 v[54:55], v[60:61], v[54:55]
	s_waitcnt lgkmcnt(0)
	v_pk_fma_f32 v[82:83], v[56:57], v[50:51], v[0:1]
	v_pk_fma_f32 v[42:43], v[18:19], v[54:55], v[42:43]
	v_pk_fma_f32 v[40:41], v[16:17], v[56:57], v[40:41]
	v_pk_fma_f32 v[38:39], v[26:27], v[54:55], v[38:39]
	v_pk_fma_f32 v[36:37], v[24:25], v[56:57], v[36:37]
	v_pk_fma_f32 v[34:35], v[30:31], v[54:55], v[34:35]
	v_pk_fma_f32 v[32:33], v[28:29], v[56:57], v[32:33]
	v_pk_fma_f32 v[22:23], v[48:49], v[54:55], v[22:23]
	v_pk_fma_f32 v[20:21], v[46:47], v[56:57], v[20:21]
	v_pk_fma_f32 v[84:85], v[52:53], v[54:55], v[2:3]
.LBB0_277:
	s_or_b64 exec, exec, s[6:7]
	v_mov_b64_e32 v[26:27], v[2:3]
	v_cmp_lt_u32_e32 vcc, 24, v44
	v_mov_b64_e32 v[24:25], v[0:1]
	s_and_saveexec_b64 s[6:7], vcc
	s_cbranch_execz .LBB0_279
	s_waitcnt vmcnt(48)
	v_mov_b64_e32 v[58:59], v[116:117]
	v_mov_b64_e32 v[60:61], v[118:119]
	ds_read_b128 v[16:19], v161 offset:9216
	ds_read_b128 v[24:27], v161 offset:8192
	ds_read_b128 v[28:31], v161 offset:7168
	ds_read_b128 v[46:49], v161 offset:6144
	ds_read_b128 v[50:53], v161 offset:5120
	ds_read_b128 v[54:57], v161 offset:4096
	v_lshlrev_b32_e32 v62, 16, v58
	v_lshlrev_b32_e32 v45, 16, v60
	v_and_b32_e32 v63, 0xffff0000, v58
	v_and_b32_e32 v58, 0xffff0000, v60
	v_lshlrev_b32_e32 v60, 16, v61
	v_and_b32_e32 v61, 0xffff0000, v61
	v_mul_f32_e32 v45, 0xbfb8aa3b, v45
	v_mul_f32_e32 v58, 0xbfb8aa3b, v58
	v_mul_f32_e32 v60, 0xbfb8aa3b, v60
	v_mul_f32_e32 v61, 0xbfb8aa3b, v61
	v_exp_f32_e32 v45, v45
	v_exp_f32_e32 v58, v58
	v_exp_f32_e32 v60, v60
	v_exp_f32_e32 v61, v61
	v_add_f32_e32 v45, 1.0, v45
	v_add_f32_e32 v58, 1.0, v58
	v_add_f32_e32 v64, 1.0, v60
	v_add_f32_e32 v65, 1.0, v61
	v_rcp_f32_e32 v60, v45
	v_rcp_f32_e32 v61, v58
	v_rcp_f32_e32 v64, v64
	v_rcp_f32_e32 v65, v65
	v_lshlrev_b32_e32 v58, 16, v59
	v_and_b32_e32 v59, 0xffff0000, v59
	v_pk_mul_f32 v[60:61], v[60:61], v[62:63]
	v_pk_mul_f32 v[58:59], v[64:65], v[58:59]
	s_waitcnt lgkmcnt(1)
	v_pk_fma_f32 v[82:83], v[60:61], v[50:51], v[82:83]
	v_pk_fma_f32 v[84:85], v[52:53], v[58:59], v[84:85]
	v_pk_fma_f32 v[42:43], v[18:19], v[58:59], v[42:43]
	v_pk_fma_f32 v[40:41], v[16:17], v[60:61], v[40:41]
	v_pk_fma_f32 v[38:39], v[26:27], v[58:59], v[38:39]
	v_pk_fma_f32 v[36:37], v[24:25], v[60:61], v[36:37]
	v_pk_fma_f32 v[34:35], v[30:31], v[58:59], v[34:35]
	v_pk_fma_f32 v[32:33], v[28:29], v[60:61], v[32:33]
	v_pk_fma_f32 v[22:23], v[48:49], v[58:59], v[22:23]
	v_pk_fma_f32 v[20:21], v[46:47], v[60:61], v[20:21]
	s_waitcnt lgkmcnt(0)
	v_pk_fma_f32 v[26:27], v[58:59], v[56:57], v[2:3]
	v_pk_fma_f32 v[24:25], v[60:61], v[54:55], v[0:1]
.LBB0_279:
	s_or_b64 exec, exec, s[6:7]
	v_mov_b64_e32 v[18:19], v[2:3]
	v_cmp_lt_u32_e32 vcc, 23, v44
	v_mov_b64_e32 v[16:17], v[0:1]
	s_and_saveexec_b64 s[6:7], vcc
	s_cbranch_execz .LBB0_281
	s_waitcnt vmcnt(46)
	v_mov_b64_e32 v[66:67], v[120:121]
	v_mov_b64_e32 v[68:69], v[122:123]
	ds_read_b128 v[16:19], v161 offset:10240
	ds_read_b128 v[28:31], v161 offset:9216
	ds_read_b128 v[46:49], v161 offset:8192
	ds_read_b128 v[50:53], v161 offset:7168
	ds_read_b128 v[54:57], v161 offset:6144
	ds_read_b128 v[58:61], v161 offset:5120
	ds_read_b128 v[62:65], v161 offset:4096
	v_lshlrev_b32_e32 v70, 16, v66
	v_lshlrev_b32_e32 v45, 16, v68
	v_and_b32_e32 v71, 0xffff0000, v66
	v_and_b32_e32 v66, 0xffff0000, v68
	v_lshlrev_b32_e32 v68, 16, v69
	v_and_b32_e32 v69, 0xffff0000, v69
	v_mul_f32_e32 v45, 0xbfb8aa3b, v45
	v_mul_f32_e32 v66, 0xbfb8aa3b, v66
	v_mul_f32_e32 v68, 0xbfb8aa3b, v68
	v_mul_f32_e32 v69, 0xbfb8aa3b, v69
	v_exp_f32_e32 v45, v45
	v_exp_f32_e32 v66, v66
	v_exp_f32_e32 v68, v68
	v_exp_f32_e32 v69, v69
	v_add_f32_e32 v45, 1.0, v45
	v_add_f32_e32 v66, 1.0, v66
	v_add_f32_e32 v72, 1.0, v68
	v_add_f32_e32 v73, 1.0, v69
	v_rcp_f32_e32 v68, v45
	v_rcp_f32_e32 v69, v66
	v_rcp_f32_e32 v72, v72
	v_rcp_f32_e32 v73, v73
	v_lshlrev_b32_e32 v66, 16, v67
	v_and_b32_e32 v67, 0xffff0000, v67
	v_pk_mul_f32 v[68:69], v[68:69], v[70:71]
	v_pk_mul_f32 v[66:67], v[72:73], v[66:67]
	s_waitcnt lgkmcnt(2)
	v_pk_fma_f32 v[82:83], v[68:69], v[54:55], v[82:83]
	v_pk_fma_f32 v[84:85], v[56:57], v[66:67], v[84:85]
	v_pk_fma_f32 v[42:43], v[18:19], v[66:67], v[42:43]
	v_pk_fma_f32 v[40:41], v[16:17], v[68:69], v[40:41]
	v_pk_fma_f32 v[38:39], v[30:31], v[66:67], v[38:39]
	v_pk_fma_f32 v[36:37], v[28:29], v[68:69], v[36:37]
	v_pk_fma_f32 v[34:35], v[48:49], v[66:67], v[34:35]
	v_pk_fma_f32 v[32:33], v[46:47], v[68:69], v[32:33]
	v_pk_fma_f32 v[22:23], v[52:53], v[66:67], v[22:23]
	v_pk_fma_f32 v[20:21], v[50:51], v[68:69], v[20:21]
	s_waitcnt lgkmcnt(1)
	v_pk_fma_f32 v[26:27], v[66:67], v[60:61], v[26:27]
	v_pk_fma_f32 v[24:25], v[68:69], v[58:59], v[24:25]
	s_waitcnt lgkmcnt(0)
	v_pk_fma_f32 v[18:19], v[66:67], v[64:65], v[2:3]
	v_pk_fma_f32 v[16:17], v[68:69], v[62:63], v[0:1]

.LBB0_303:
	s_waitcnt vmcnt(2)
	v_mov_b64_e32 v[86:87], v[238:239]
	v_mov_b64_e32 v[88:89], v[240:241]
	ds_read_b128 v[68:71], v161 offset:26624
	ds_read_b128 v[72:75], v161 offset:25600
	v_lshlrev_b32_e32 v90, 16, v86
	v_lshlrev_b32_e32 v81, 16, v88
	v_and_b32_e32 v91, 0xffff0000, v86
	v_and_b32_e32 v86, 0xffff0000, v88
	v_lshlrev_b32_e32 v88, 16, v89
	v_and_b32_e32 v89, 0xffff0000, v89
	v_mul_f32_e32 v81, 0xbfb8aa3b, v81
	v_mul_f32_e32 v86, 0xbfb8aa3b, v86
	v_mul_f32_e32 v88, 0xbfb8aa3b, v88
	v_mul_f32_e32 v89, 0xbfb8aa3b, v89
	v_exp_f32_e32 v81, v81
	v_exp_f32_e32 v86, v86
	v_exp_f32_e32 v88, v88
	v_exp_f32_e32 v89, v89
	v_add_f32_e32 v81, 1.0, v81
	v_add_f32_e32 v86, 1.0, v86
	v_add_f32_e32 v92, 1.0, v88
	v_add_f32_e32 v93, 1.0, v89
	v_rcp_f32_e32 v88, v81
	v_rcp_f32_e32 v89, v86
	v_rcp_f32_e32 v92, v92
	v_rcp_f32_e32 v93, v93
	v_lshlrev_b32_e32 v86, 16, v87
	v_and_b32_e32 v87, 0xffff0000, v87
	v_pk_mul_f32 v[88:89], v[88:89], v[90:91]
	v_pk_mul_f32 v[86:87], v[92:93], v[86:87]
	s_waitcnt lgkmcnt(6)
	v_pk_fma_f32 v[82:83], v[88:89], v[48:49], v[82:83]
	v_pk_fma_f32 v[84:85], v[50:51], v[86:87], v[84:85]
	s_waitcnt lgkmcnt(2)
	v_pk_fma_f32 v[42:43], v[66:67], v[86:87], v[42:43]
	v_pk_fma_f32 v[40:41], v[64:65], v[88:89], v[40:41]
	v_pk_fma_f32 v[38:39], v[62:63], v[86:87], v[38:39]
	v_pk_fma_f32 v[36:37], v[60:61], v[88:89], v[36:37]
	v_pk_fma_f32 v[34:35], v[58:59], v[86:87], v[34:35]
	v_pk_fma_f32 v[32:33], v[56:57], v[88:89], v[32:33]
	v_pk_fma_f32 v[22:23], v[54:55], v[86:87], v[22:23]
	v_pk_fma_f32 v[20:21], v[52:53], v[88:89], v[20:21]
	v_pk_fma_f32 v[26:27], v[86:87], v[46:47], v[26:27]
	v_pk_fma_f32 v[24:25], v[88:89], v[44:45], v[24:25]
	s_waitcnt lgkmcnt(1)
	v_pk_fma_f32 v[18:19], v[86:87], v[70:71], v[18:19]
	v_pk_fma_f32 v[16:17], v[88:89], v[68:69], v[16:17]
	s_waitcnt lgkmcnt(0)
	v_pk_fma_f32 v[30:31], v[86:87], v[74:75], v[30:31]
	v_pk_fma_f32 v[28:29], v[88:89], v[72:73], v[28:29]
.LBB0_304:
	s_or_b64 exec, exec, s[6:7]
	ds_read_b128 v[68:71], v161 offset:33792
	s_and_saveexec_b64 s[6:7], vcc
	s_xor_b64 s[6:7], exec, s[6:7]
	s_cbranch_execz .LBB0_266
	s_waitcnt vmcnt(0)
	v_mov_b64_e32 v[86:87], v[242:243]
	v_mov_b64_e32 v[88:89], v[244:245]
	ds_read_b128 v[72:75], v161 offset:26624
	v_lshlrev_b32_e32 v90, 16, v86
	v_lshlrev_b32_e32 v81, 16, v88
	v_and_b32_e32 v91, 0xffff0000, v86
	v_and_b32_e32 v86, 0xffff0000, v88
	v_lshlrev_b32_e32 v88, 16, v89
	v_and_b32_e32 v89, 0xffff0000, v89
	v_mul_f32_e32 v81, 0xbfb8aa3b, v81
	v_mul_f32_e32 v86, 0xbfb8aa3b, v86
	v_mul_f32_e32 v88, 0xbfb8aa3b, v88
	v_mul_f32_e32 v89, 0xbfb8aa3b, v89
	v_exp_f32_e32 v81, v81
	v_exp_f32_e32 v86, v86
	v_exp_f32_e32 v88, v88
	v_exp_f32_e32 v89, v89
	v_add_f32_e32 v81, 1.0, v81
	v_add_f32_e32 v86, 1.0, v86
	v_add_f32_e32 v92, 1.0, v88
	v_add_f32_e32 v93, 1.0, v89
	v_rcp_f32_e32 v88, v81
	v_rcp_f32_e32 v89, v86
	v_rcp_f32_e32 v92, v92
	v_rcp_f32_e32 v93, v93
	v_lshlrev_b32_e32 v86, 16, v87
	v_and_b32_e32 v87, 0xffff0000, v87
	v_pk_mul_f32 v[88:89], v[88:89], v[90:91]
	v_pk_mul_f32 v[86:87], v[92:93], v[86:87]
	s_waitcnt lgkmcnt(5)
	v_pk_fma_f32 v[82:83], v[88:89], v[52:53], v[82:83]
	v_pk_fma_f32 v[84:85], v[54:55], v[86:87], v[84:85]
	s_waitcnt lgkmcnt(1)
	v_pk_fma_f32 v[42:43], v[70:71], v[86:87], v[42:43]
	v_pk_fma_f32 v[40:41], v[68:69], v[88:89], v[40:41]
	v_pk_fma_f32 v[38:39], v[66:67], v[86:87], v[38:39]
	v_pk_fma_f32 v[36:37], v[64:65], v[88:89], v[36:37]
	v_pk_fma_f32 v[34:35], v[62:63], v[86:87], v[34:35]
	v_pk_fma_f32 v[32:33], v[60:61], v[88:89], v[32:33]
	v_pk_fma_f32 v[22:23], v[58:59], v[86:87], v[22:23]
	v_pk_fma_f32 v[20:21], v[56:57], v[88:89], v[20:21]
	v_pk_fma_f32 v[26:27], v[86:87], v[50:51], v[26:27]
	v_pk_fma_f32 v[24:25], v[88:89], v[48:49], v[24:25]
	v_pk_fma_f32 v[18:19], v[86:87], v[46:47], v[18:19]
	v_pk_fma_f32 v[16:17], v[88:89], v[44:45], v[16:17]
	s_waitcnt lgkmcnt(0)
	v_pk_fma_f32 v[30:31], v[86:87], v[74:75], v[30:31]
	v_pk_fma_f32 v[28:29], v[88:89], v[72:73], v[28:29]
	s_branch .LBB0_266
.LBB0_306:
	s_waitcnt vmcnt(44)
	v_mov_b64_e32 v[74:75], v[124:125]
	v_mov_b64_e32 v[86:87], v[126:127]
	ds_read_b128 v[28:31], v161 offset:11264
	ds_read_b128 v[46:49], v161 offset:10240
	ds_read_b128 v[50:53], v161 offset:9216
	ds_read_b128 v[54:57], v161 offset:8192
	ds_read_b128 v[58:61], v161 offset:7168
	ds_read_b128 v[62:65], v161 offset:6144
	ds_read_b128 v[66:69], v161 offset:5120
	ds_read_b128 v[70:73], v161 offset:4096
	v_lshlrev_b32_e32 v88, 16, v74
	v_lshlrev_b32_e32 v45, 16, v86
	v_and_b32_e32 v89, 0xffff0000, v74
	v_and_b32_e32 v74, 0xffff0000, v86
	v_lshlrev_b32_e32 v81, 16, v87
	v_and_b32_e32 v86, 0xffff0000, v87
	v_mul_f32_e32 v45, 0xbfb8aa3b, v45
	v_mul_f32_e32 v74, 0xbfb8aa3b, v74
	v_mul_f32_e32 v81, 0xbfb8aa3b, v81
	v_mul_f32_e32 v86, 0xbfb8aa3b, v86
	v_exp_f32_e32 v45, v45
	v_exp_f32_e32 v74, v74
	v_exp_f32_e32 v81, v81
	v_exp_f32_e32 v86, v86
	v_add_f32_e32 v45, 1.0, v45
	v_add_f32_e32 v74, 1.0, v74
	v_add_f32_e32 v81, 1.0, v81
	v_add_f32_e32 v91, 1.0, v86
	v_rcp_f32_e32 v86, v45
	v_rcp_f32_e32 v87, v74
	v_rcp_f32_e32 v90, v81
	v_rcp_f32_e32 v91, v91
	v_lshlrev_b32_e32 v74, 16, v75
	v_and_b32_e32 v75, 0xffff0000, v75
	v_pk_mul_f32 v[86:87], v[86:87], v[88:89]
	v_pk_mul_f32 v[74:75], v[90:91], v[74:75]
	s_waitcnt lgkmcnt(3)
	v_pk_fma_f32 v[82:83], v[86:87], v[58:59], v[82:83]
	v_pk_fma_f32 v[84:85], v[60:61], v[74:75], v[84:85]
	v_pk_fma_f32 v[42:43], v[30:31], v[74:75], v[42:43]
	v_pk_fma_f32 v[40:41], v[28:29], v[86:87], v[40:41]
	v_pk_fma_f32 v[38:39], v[48:49], v[74:75], v[38:39]
	v_pk_fma_f32 v[36:37], v[46:47], v[86:87], v[36:37]
	v_pk_fma_f32 v[34:35], v[52:53], v[74:75], v[34:35]
	v_pk_fma_f32 v[32:33], v[50:51], v[86:87], v[32:33]
	v_pk_fma_f32 v[22:23], v[56:57], v[74:75], v[22:23]
	v_pk_fma_f32 v[20:21], v[54:55], v[86:87], v[20:21]
	s_waitcnt lgkmcnt(2)
	v_pk_fma_f32 v[26:27], v[74:75], v[64:65], v[26:27]
	v_pk_fma_f32 v[24:25], v[86:87], v[62:63], v[24:25]
	s_waitcnt lgkmcnt(1)
	v_pk_fma_f32 v[18:19], v[74:75], v[68:69], v[18:19]
	v_pk_fma_f32 v[16:17], v[86:87], v[66:67], v[16:17]
	s_waitcnt lgkmcnt(0)
	v_pk_fma_f32 v[30:31], v[74:75], v[72:73], v[2:3]
	v_pk_fma_f32 v[28:29], v[86:87], v[70:71], v[0:1]
	s_or_b64 exec, exec, s[6:7]
	v_cmp_lt_u32_e32 vcc, 21, v44
	s_and_saveexec_b64 s[6:7], vcc
	s_cbranch_execz .LBB0_283
.LBB0_307:
	s_waitcnt vmcnt(42)
	v_mov_b64_e32 v[74:75], v[128:129]
	v_mov_b64_e32 v[90:91], v[130:131]
	ds_read_b128 v[46:49], v161 offset:12288
	ds_read_b128 v[50:53], v161 offset:11264
	ds_read_b128 v[54:57], v161 offset:10240
	ds_read_b128 v[58:61], v161 offset:9216
	ds_read_b128 v[62:65], v161 offset:8192
	ds_read_b128 v[66:69], v161 offset:7168
	ds_read_b128 v[70:73], v161 offset:6144
	ds_read_b128 v[86:89], v161 offset:5120
	v_lshlrev_b32_e32 v92, 16, v74
	v_lshlrev_b32_e32 v45, 16, v90
	v_and_b32_e32 v93, 0xffff0000, v74
	v_and_b32_e32 v74, 0xffff0000, v90
	v_lshlrev_b32_e32 v81, 16, v91
	v_and_b32_e32 v90, 0xffff0000, v91
	v_mul_f32_e32 v45, 0xbfb8aa3b, v45
	v_mul_f32_e32 v74, 0xbfb8aa3b, v74
	v_mul_f32_e32 v81, 0xbfb8aa3b, v81
	v_mul_f32_e32 v90, 0xbfb8aa3b, v90
	v_exp_f32_e32 v45, v45
	v_exp_f32_e32 v74, v74
	v_exp_f32_e32 v81, v81
	v_exp_f32_e32 v90, v90
	v_add_f32_e32 v45, 1.0, v45
	v_add_f32_e32 v74, 1.0, v74
	v_add_f32_e32 v81, 1.0, v81
	v_add_f32_e32 v95, 1.0, v90
	v_rcp_f32_e32 v90, v45
	v_rcp_f32_e32 v91, v74
	v_rcp_f32_e32 v94, v81
	v_rcp_f32_e32 v95, v95
	v_lshlrev_b32_e32 v74, 16, v75
	v_and_b32_e32 v75, 0xffff0000, v75
	v_pk_mul_f32 v[90:91], v[90:91], v[92:93]
	v_pk_mul_f32 v[74:75], v[94:95], v[74:75]
	s_waitcnt lgkmcnt(3)
	v_pk_fma_f32 v[82:83], v[90:91], v[62:63], v[82:83]
	v_pk_fma_f32 v[84:85], v[64:65], v[74:75], v[84:85]
	v_pk_fma_f32 v[42:43], v[48:49], v[74:75], v[42:43]
	v_pk_fma_f32 v[40:41], v[46:47], v[90:91], v[40:41]
	v_pk_fma_f32 v[38:39], v[52:53], v[74:75], v[38:39]
	v_pk_fma_f32 v[36:37], v[50:51], v[90:91], v[36:37]
	v_pk_fma_f32 v[34:35], v[56:57], v[74:75], v[34:35]
	v_pk_fma_f32 v[32:33], v[54:55], v[90:91], v[32:33]
	v_pk_fma_f32 v[22:23], v[60:61], v[74:75], v[22:23]
	v_pk_fma_f32 v[20:21], v[58:59], v[90:91], v[20:21]
	s_waitcnt lgkmcnt(2)
	v_pk_fma_f32 v[26:27], v[74:75], v[68:69], v[26:27]
	v_pk_fma_f32 v[24:25], v[90:91], v[66:67], v[24:25]
	s_waitcnt lgkmcnt(1)
	v_pk_fma_f32 v[18:19], v[74:75], v[72:73], v[18:19]
	v_pk_fma_f32 v[16:17], v[90:91], v[70:71], v[16:17]
	s_waitcnt lgkmcnt(0)
	v_pk_fma_f32 v[30:31], v[74:75], v[88:89], v[30:31]
	v_pk_fma_f32 v[28:29], v[90:91], v[86:87], v[28:29]
	s_or_b64 exec, exec, s[6:7]
	v_cmp_lt_u32_e32 vcc, 20, v44
	s_and_saveexec_b64 s[6:7], vcc
	s_cbranch_execz .LBB0_284
.LBB0_308:
	s_waitcnt vmcnt(40)
	v_mov_b64_e32 v[74:75], v[132:133]
	v_mov_b64_e32 v[90:91], v[134:135]
	ds_read_b128 v[46:49], v161 offset:13312
	ds_read_b128 v[50:53], v161 offset:12288
	ds_read_b128 v[54:57], v161 offset:11264
	ds_read_b128 v[58:61], v161 offset:10240
	ds_read_b128 v[62:65], v161 offset:9216
	ds_read_b128 v[66:69], v161 offset:8192
	ds_read_b128 v[70:73], v161 offset:7168
	ds_read_b128 v[86:89], v161 offset:6144
	v_lshlrev_b32_e32 v92, 16, v74
	v_lshlrev_b32_e32 v45, 16, v90
	v_and_b32_e32 v93, 0xffff0000, v74
	v_and_b32_e32 v74, 0xffff0000, v90
	v_lshlrev_b32_e32 v81, 16, v91
	v_and_b32_e32 v90, 0xffff0000, v91
	v_mul_f32_e32 v45, 0xbfb8aa3b, v45
	v_mul_f32_e32 v74, 0xbfb8aa3b, v74
	v_mul_f32_e32 v81, 0xbfb8aa3b, v81
	v_mul_f32_e32 v90, 0xbfb8aa3b, v90
	v_exp_f32_e32 v45, v45
	v_exp_f32_e32 v74, v74
	v_exp_f32_e32 v81, v81
	v_exp_f32_e32 v90, v90
	v_add_f32_e32 v45, 1.0, v45
	v_add_f32_e32 v74, 1.0, v74
	v_add_f32_e32 v81, 1.0, v81
	v_add_f32_e32 v95, 1.0, v90
	v_rcp_f32_e32 v90, v45
	v_rcp_f32_e32 v91, v74
	v_rcp_f32_e32 v94, v81
	v_rcp_f32_e32 v95, v95
	v_lshlrev_b32_e32 v74, 16, v75
	v_and_b32_e32 v75, 0xffff0000, v75
	v_pk_mul_f32 v[90:91], v[90:91], v[92:93]
	v_pk_mul_f32 v[74:75], v[94:95], v[74:75]
	s_waitcnt lgkmcnt(3)
	v_pk_fma_f32 v[82:83], v[90:91], v[62:63], v[82:83]
	v_pk_fma_f32 v[84:85], v[64:65], v[74:75], v[84:85]
	v_pk_fma_f32 v[42:43], v[48:49], v[74:75], v[42:43]
	v_pk_fma_f32 v[40:41], v[46:47], v[90:91], v[40:41]
	v_pk_fma_f32 v[38:39], v[52:53], v[74:75], v[38:39]
	v_pk_fma_f32 v[36:37], v[50:51], v[90:91], v[36:37]
	v_pk_fma_f32 v[34:35], v[56:57], v[74:75], v[34:35]
	v_pk_fma_f32 v[32:33], v[54:55], v[90:91], v[32:33]
	v_pk_fma_f32 v[22:23], v[60:61], v[74:75], v[22:23]
	v_pk_fma_f32 v[20:21], v[58:59], v[90:91], v[20:21]
	s_waitcnt lgkmcnt(2)
	v_pk_fma_f32 v[26:27], v[74:75], v[68:69], v[26:27]
	v_pk_fma_f32 v[24:25], v[90:91], v[66:67], v[24:25]
	s_waitcnt lgkmcnt(1)
	v_pk_fma_f32 v[18:19], v[74:75], v[72:73], v[18:19]
	v_pk_fma_f32 v[16:17], v[90:91], v[70:71], v[16:17]
	s_waitcnt lgkmcnt(0)
	v_pk_fma_f32 v[30:31], v[74:75], v[88:89], v[30:31]
	v_pk_fma_f32 v[28:29], v[90:91], v[86:87], v[28:29]
	s_or_b64 exec, exec, s[6:7]
	v_cmp_lt_u32_e32 vcc, 19, v44
	s_and_saveexec_b64 s[6:7], vcc
	s_cbranch_execz .LBB0_285
.LBB0_309:
	s_waitcnt vmcnt(38)
	v_mov_b64_e32 v[74:75], v[136:137]
	v_mov_b64_e32 v[90:91], v[138:139]
	ds_read_b128 v[46:49], v161 offset:14336
	ds_read_b128 v[50:53], v161 offset:13312
	ds_read_b128 v[54:57], v161 offset:12288
	ds_read_b128 v[58:61], v161 offset:11264
	ds_read_b128 v[62:65], v161 offset:10240
	ds_read_b128 v[66:69], v161 offset:9216
	ds_read_b128 v[70:73], v161 offset:8192
	ds_read_b128 v[86:89], v161 offset:7168
	v_lshlrev_b32_e32 v92, 16, v74
	v_lshlrev_b32_e32 v45, 16, v90
	v_and_b32_e32 v93, 0xffff0000, v74
	v_and_b32_e32 v74, 0xffff0000, v90
	v_lshlrev_b32_e32 v81, 16, v91
	v_and_b32_e32 v90, 0xffff0000, v91
	v_mul_f32_e32 v45, 0xbfb8aa3b, v45
	v_mul_f32_e32 v74, 0xbfb8aa3b, v74
	v_mul_f32_e32 v81, 0xbfb8aa3b, v81
	v_mul_f32_e32 v90, 0xbfb8aa3b, v90
	v_exp_f32_e32 v45, v45
	v_exp_f32_e32 v74, v74
	v_exp_f32_e32 v81, v81
	v_exp_f32_e32 v90, v90
	v_add_f32_e32 v45, 1.0, v45
	v_add_f32_e32 v74, 1.0, v74
	v_add_f32_e32 v81, 1.0, v81
	v_add_f32_e32 v95, 1.0, v90
	v_rcp_f32_e32 v90, v45
	v_rcp_f32_e32 v91, v74
	v_rcp_f32_e32 v94, v81
	v_rcp_f32_e32 v95, v95
	v_lshlrev_b32_e32 v74, 16, v75
	v_and_b32_e32 v75, 0xffff0000, v75
	v_pk_mul_f32 v[90:91], v[90:91], v[92:93]
	v_pk_mul_f32 v[74:75], v[94:95], v[74:75]
	s_waitcnt lgkmcnt(3)
	v_pk_fma_f32 v[82:83], v[90:91], v[62:63], v[82:83]
	v_pk_fma_f32 v[84:85], v[64:65], v[74:75], v[84:85]
	v_pk_fma_f32 v[42:43], v[48:49], v[74:75], v[42:43]
	v_pk_fma_f32 v[40:41], v[46:47], v[90:91], v[40:41]
	v_pk_fma_f32 v[38:39], v[52:53], v[74:75], v[38:39]
	v_pk_fma_f32 v[36:37], v[50:51], v[90:91], v[36:37]
	v_pk_fma_f32 v[34:35], v[56:57], v[74:75], v[34:35]
	v_pk_fma_f32 v[32:33], v[54:55], v[90:91], v[32:33]
	v_pk_fma_f32 v[22:23], v[60:61], v[74:75], v[22:23]
	v_pk_fma_f32 v[20:21], v[58:59], v[90:91], v[20:21]
	s_waitcnt lgkmcnt(2)
	v_pk_fma_f32 v[26:27], v[74:75], v[68:69], v[26:27]
	v_pk_fma_f32 v[24:25], v[90:91], v[66:67], v[24:25]
	s_waitcnt lgkmcnt(1)
	v_pk_fma_f32 v[18:19], v[74:75], v[72:73], v[18:19]
	v_pk_fma_f32 v[16:17], v[90:91], v[70:71], v[16:17]
	s_waitcnt lgkmcnt(0)
	v_pk_fma_f32 v[30:31], v[74:75], v[88:89], v[30:31]
	v_pk_fma_f32 v[28:29], v[90:91], v[86:87], v[28:29]
	s_or_b64 exec, exec, s[6:7]
	v_cmp_lt_u32_e32 vcc, 18, v44
	s_and_saveexec_b64 s[6:7], vcc
	s_cbranch_execz .LBB0_286
.LBB0_310:
	s_waitcnt vmcnt(36)
	v_mov_b64_e32 v[74:75], v[140:141]
	v_mov_b64_e32 v[90:91], v[142:143]
	ds_read_b128 v[46:49], v161 offset:15360
	ds_read_b128 v[50:53], v161 offset:14336
	ds_read_b128 v[54:57], v161 offset:13312
	ds_read_b128 v[58:61], v161 offset:12288
	ds_read_b128 v[62:65], v161 offset:11264
	ds_read_b128 v[66:69], v161 offset:10240
	ds_read_b128 v[70:73], v161 offset:9216
	ds_read_b128 v[86:89], v161 offset:8192
	v_lshlrev_b32_e32 v92, 16, v74
	v_lshlrev_b32_e32 v45, 16, v90
	v_and_b32_e32 v93, 0xffff0000, v74
	v_and_b32_e32 v74, 0xffff0000, v90
	v_lshlrev_b32_e32 v81, 16, v91
	v_and_b32_e32 v90, 0xffff0000, v91
	v_mul_f32_e32 v45, 0xbfb8aa3b, v45
	v_mul_f32_e32 v74, 0xbfb8aa3b, v74
	v_mul_f32_e32 v81, 0xbfb8aa3b, v81
	v_mul_f32_e32 v90, 0xbfb8aa3b, v90
	v_exp_f32_e32 v45, v45
	v_exp_f32_e32 v74, v74
	v_exp_f32_e32 v81, v81
	v_exp_f32_e32 v90, v90
	v_add_f32_e32 v45, 1.0, v45
	v_add_f32_e32 v74, 1.0, v74
	v_add_f32_e32 v81, 1.0, v81
	v_add_f32_e32 v95, 1.0, v90
	v_rcp_f32_e32 v90, v45
	v_rcp_f32_e32 v91, v74
	v_rcp_f32_e32 v94, v81
	v_rcp_f32_e32 v95, v95
	v_lshlrev_b32_e32 v74, 16, v75
	v_and_b32_e32 v75, 0xffff0000, v75
	v_pk_mul_f32 v[90:91], v[90:91], v[92:93]
	v_pk_mul_f32 v[74:75], v[94:95], v[74:75]
	s_waitcnt lgkmcnt(3)
	v_pk_fma_f32 v[82:83], v[90:91], v[62:63], v[82:83]
	v_pk_fma_f32 v[84:85], v[64:65], v[74:75], v[84:85]
	v_pk_fma_f32 v[42:43], v[48:49], v[74:75], v[42:43]
	v_pk_fma_f32 v[40:41], v[46:47], v[90:91], v[40:41]
	v_pk_fma_f32 v[38:39], v[52:53], v[74:75], v[38:39]
	v_pk_fma_f32 v[36:37], v[50:51], v[90:91], v[36:37]
	v_pk_fma_f32 v[34:35], v[56:57], v[74:75], v[34:35]
	v_pk_fma_f32 v[32:33], v[54:55], v[90:91], v[32:33]
	v_pk_fma_f32 v[22:23], v[60:61], v[74:75], v[22:23]
	v_pk_fma_f32 v[20:21], v[58:59], v[90:91], v[20:21]
	s_waitcnt lgkmcnt(2)
	v_pk_fma_f32 v[26:27], v[74:75], v[68:69], v[26:27]
	v_pk_fma_f32 v[24:25], v[90:91], v[66:67], v[24:25]
	s_waitcnt lgkmcnt(1)
	v_pk_fma_f32 v[18:19], v[74:75], v[72:73], v[18:19]
	v_pk_fma_f32 v[16:17], v[90:91], v[70:71], v[16:17]
	s_waitcnt lgkmcnt(0)
	v_pk_fma_f32 v[30:31], v[74:75], v[88:89], v[30:31]
	v_pk_fma_f32 v[28:29], v[90:91], v[86:87], v[28:29]
	s_or_b64 exec, exec, s[6:7]
	v_cmp_lt_u32_e32 vcc, 17, v44
	s_and_saveexec_b64 s[6:7], vcc
	s_cbranch_execz .LBB0_287
.LBB0_311:
	s_waitcnt vmcnt(34)
	v_mov_b64_e32 v[74:75], v[152:153]
	v_mov_b64_e32 v[90:91], v[154:155]
	ds_read_b128 v[46:49], v161 offset:16384
	ds_read_b128 v[50:53], v161 offset:15360
	ds_read_b128 v[54:57], v161 offset:14336
	ds_read_b128 v[58:61], v161 offset:13312
	ds_read_b128 v[62:65], v161 offset:12288
	ds_read_b128 v[66:69], v161 offset:11264
	ds_read_b128 v[70:73], v161 offset:10240
	ds_read_b128 v[86:89], v161 offset:9216
	v_lshlrev_b32_e32 v92, 16, v74
	v_lshlrev_b32_e32 v45, 16, v90
	v_and_b32_e32 v93, 0xffff0000, v74
	v_and_b32_e32 v74, 0xffff0000, v90
	v_lshlrev_b32_e32 v81, 16, v91
	v_and_b32_e32 v90, 0xffff0000, v91
	v_mul_f32_e32 v45, 0xbfb8aa3b, v45
	v_mul_f32_e32 v74, 0xbfb8aa3b, v74
	v_mul_f32_e32 v81, 0xbfb8aa3b, v81
	v_mul_f32_e32 v90, 0xbfb8aa3b, v90
	v_exp_f32_e32 v45, v45
	v_exp_f32_e32 v74, v74
	v_exp_f32_e32 v81, v81
	v_exp_f32_e32 v90, v90
	v_add_f32_e32 v45, 1.0, v45
	v_add_f32_e32 v74, 1.0, v74
	v_add_f32_e32 v81, 1.0, v81
	v_add_f32_e32 v95, 1.0, v90
	v_rcp_f32_e32 v90, v45
	v_rcp_f32_e32 v91, v74
	v_rcp_f32_e32 v94, v81
	v_rcp_f32_e32 v95, v95
	v_lshlrev_b32_e32 v74, 16, v75
	v_and_b32_e32 v75, 0xffff0000, v75
	v_pk_mul_f32 v[90:91], v[90:91], v[92:93]
	v_pk_mul_f32 v[74:75], v[94:95], v[74:75]
	s_waitcnt lgkmcnt(3)
	v_pk_fma_f32 v[82:83], v[90:91], v[62:63], v[82:83]
	v_pk_fma_f32 v[84:85], v[64:65], v[74:75], v[84:85]
	v_pk_fma_f32 v[42:43], v[48:49], v[74:75], v[42:43]
	v_pk_fma_f32 v[40:41], v[46:47], v[90:91], v[40:41]
	v_pk_fma_f32 v[38:39], v[52:53], v[74:75], v[38:39]
	v_pk_fma_f32 v[36:37], v[50:51], v[90:91], v[36:37]
	v_pk_fma_f32 v[34:35], v[56:57], v[74:75], v[34:35]
	v_pk_fma_f32 v[32:33], v[54:55], v[90:91], v[32:33]
	v_pk_fma_f32 v[22:23], v[60:61], v[74:75], v[22:23]
	v_pk_fma_f32 v[20:21], v[58:59], v[90:91], v[20:21]
	s_waitcnt lgkmcnt(2)
	v_pk_fma_f32 v[26:27], v[74:75], v[68:69], v[26:27]
	v_pk_fma_f32 v[24:25], v[90:91], v[66:67], v[24:25]
	s_waitcnt lgkmcnt(1)
	v_pk_fma_f32 v[18:19], v[74:75], v[72:73], v[18:19]
	v_pk_fma_f32 v[16:17], v[90:91], v[70:71], v[16:17]
	s_waitcnt lgkmcnt(0)
	v_pk_fma_f32 v[30:31], v[74:75], v[88:89], v[30:31]
	v_pk_fma_f32 v[28:29], v[90:91], v[86:87], v[28:29]
	s_or_b64 exec, exec, s[6:7]
	v_cmp_lt_u32_e32 vcc, 16, v44
	s_and_saveexec_b64 s[6:7], vcc
	s_cbranch_execz .LBB0_288
.LBB0_312:
	s_waitcnt vmcnt(32)
	v_mov_b64_e32 v[74:75], v[156:157]
	v_mov_b64_e32 v[90:91], v[158:159]
	ds_read_b128 v[46:49], v161 offset:17408
	ds_read_b128 v[50:53], v161 offset:16384
	ds_read_b128 v[54:57], v161 offset:15360
	ds_read_b128 v[58:61], v161 offset:14336
	ds_read_b128 v[62:65], v161 offset:13312
	ds_read_b128 v[66:69], v161 offset:12288
	ds_read_b128 v[70:73], v161 offset:11264
	ds_read_b128 v[86:89], v161 offset:10240
	v_lshlrev_b32_e32 v92, 16, v74
	v_lshlrev_b32_e32 v45, 16, v90
	v_and_b32_e32 v93, 0xffff0000, v74
	v_and_b32_e32 v74, 0xffff0000, v90
	v_lshlrev_b32_e32 v81, 16, v91
	v_and_b32_e32 v90, 0xffff0000, v91
	v_mul_f32_e32 v45, 0xbfb8aa3b, v45
	v_mul_f32_e32 v74, 0xbfb8aa3b, v74
	v_mul_f32_e32 v81, 0xbfb8aa3b, v81
	v_mul_f32_e32 v90, 0xbfb8aa3b, v90
	v_exp_f32_e32 v45, v45
	v_exp_f32_e32 v74, v74
	v_exp_f32_e32 v81, v81
	v_exp_f32_e32 v90, v90
	v_add_f32_e32 v45, 1.0, v45
	v_add_f32_e32 v74, 1.0, v74
	v_add_f32_e32 v81, 1.0, v81
	v_add_f32_e32 v95, 1.0, v90
	v_rcp_f32_e32 v90, v45
	v_rcp_f32_e32 v91, v74
	v_rcp_f32_e32 v94, v81
	v_rcp_f32_e32 v95, v95
	v_lshlrev_b32_e32 v74, 16, v75
	v_and_b32_e32 v75, 0xffff0000, v75
	v_pk_mul_f32 v[90:91], v[90:91], v[92:93]
	v_pk_mul_f32 v[74:75], v[94:95], v[74:75]
	s_waitcnt lgkmcnt(3)
	v_pk_fma_f32 v[82:83], v[90:91], v[62:63], v[82:83]
	v_pk_fma_f32 v[84:85], v[64:65], v[74:75], v[84:85]
	v_pk_fma_f32 v[42:43], v[48:49], v[74:75], v[42:43]
	v_pk_fma_f32 v[40:41], v[46:47], v[90:91], v[40:41]
	v_pk_fma_f32 v[38:39], v[52:53], v[74:75], v[38:39]
	v_pk_fma_f32 v[36:37], v[50:51], v[90:91], v[36:37]
	v_pk_fma_f32 v[34:35], v[56:57], v[74:75], v[34:35]
	v_pk_fma_f32 v[32:33], v[54:55], v[90:91], v[32:33]
	v_pk_fma_f32 v[22:23], v[60:61], v[74:75], v[22:23]
	v_pk_fma_f32 v[20:21], v[58:59], v[90:91], v[20:21]
	s_waitcnt lgkmcnt(2)
	v_pk_fma_f32 v[26:27], v[74:75], v[68:69], v[26:27]
	v_pk_fma_f32 v[24:25], v[90:91], v[66:67], v[24:25]
	s_waitcnt lgkmcnt(1)
	v_pk_fma_f32 v[18:19], v[74:75], v[72:73], v[18:19]
	v_pk_fma_f32 v[16:17], v[90:91], v[70:71], v[16:17]
	s_waitcnt lgkmcnt(0)
	v_pk_fma_f32 v[30:31], v[74:75], v[88:89], v[30:31]
	v_pk_fma_f32 v[28:29], v[90:91], v[86:87], v[28:29]
	s_or_b64 exec, exec, s[6:7]
	v_cmp_lt_u32_e32 vcc, 15, v44
	s_and_saveexec_b64 s[6:7], vcc
	s_cbranch_execz .LBB0_289
.LBB0_313:
	s_waitcnt vmcnt(30)
	v_mov_b64_e32 v[74:75], v[162:163]
	v_mov_b64_e32 v[90:91], v[164:165]
	ds_read_b128 v[46:49], v161 offset:18432
	ds_read_b128 v[50:53], v161 offset:17408
	ds_read_b128 v[54:57], v161 offset:16384
	ds_read_b128 v[58:61], v161 offset:15360
	ds_read_b128 v[62:65], v161 offset:14336
	ds_read_b128 v[66:69], v161 offset:13312
	ds_read_b128 v[70:73], v161 offset:12288
	ds_read_b128 v[86:89], v161 offset:11264
	v_lshlrev_b32_e32 v92, 16, v74
	v_lshlrev_b32_e32 v45, 16, v90
	v_and_b32_e32 v93, 0xffff0000, v74
	v_and_b32_e32 v74, 0xffff0000, v90
	v_lshlrev_b32_e32 v81, 16, v91
	v_and_b32_e32 v90, 0xffff0000, v91
	v_mul_f32_e32 v45, 0xbfb8aa3b, v45
	v_mul_f32_e32 v74, 0xbfb8aa3b, v74
	v_mul_f32_e32 v81, 0xbfb8aa3b, v81
	v_mul_f32_e32 v90, 0xbfb8aa3b, v90
	v_exp_f32_e32 v45, v45
	v_exp_f32_e32 v74, v74
	v_exp_f32_e32 v81, v81
	v_exp_f32_e32 v90, v90
	v_add_f32_e32 v45, 1.0, v45
	v_add_f32_e32 v74, 1.0, v74
	v_add_f32_e32 v81, 1.0, v81
	v_add_f32_e32 v95, 1.0, v90
	v_rcp_f32_e32 v90, v45
	v_rcp_f32_e32 v91, v74
	v_rcp_f32_e32 v94, v81
	v_rcp_f32_e32 v95, v95
	v_lshlrev_b32_e32 v74, 16, v75
	v_and_b32_e32 v75, 0xffff0000, v75
	v_pk_mul_f32 v[90:91], v[90:91], v[92:93]
	v_pk_mul_f32 v[74:75], v[94:95], v[74:75]
	s_waitcnt lgkmcnt(3)
	v_pk_fma_f32 v[82:83], v[90:91], v[62:63], v[82:83]
	v_pk_fma_f32 v[84:85], v[64:65], v[74:75], v[84:85]
	v_pk_fma_f32 v[42:43], v[48:49], v[74:75], v[42:43]
	v_pk_fma_f32 v[40:41], v[46:47], v[90:91], v[40:41]
	v_pk_fma_f32 v[38:39], v[52:53], v[74:75], v[38:39]
	v_pk_fma_f32 v[36:37], v[50:51], v[90:91], v[36:37]
	v_pk_fma_f32 v[34:35], v[56:57], v[74:75], v[34:35]
	v_pk_fma_f32 v[32:33], v[54:55], v[90:91], v[32:33]
	v_pk_fma_f32 v[22:23], v[60:61], v[74:75], v[22:23]
	v_pk_fma_f32 v[20:21], v[58:59], v[90:91], v[20:21]
	s_waitcnt lgkmcnt(2)
	v_pk_fma_f32 v[26:27], v[74:75], v[68:69], v[26:27]
	v_pk_fma_f32 v[24:25], v[90:91], v[66:67], v[24:25]
	s_waitcnt lgkmcnt(1)
	v_pk_fma_f32 v[18:19], v[74:75], v[72:73], v[18:19]
	v_pk_fma_f32 v[16:17], v[90:91], v[70:71], v[16:17]
	s_waitcnt lgkmcnt(0)
	v_pk_fma_f32 v[30:31], v[74:75], v[88:89], v[30:31]
	v_pk_fma_f32 v[28:29], v[90:91], v[86:87], v[28:29]
	s_or_b64 exec, exec, s[6:7]
	v_cmp_lt_u32_e32 vcc, 14, v44
	s_and_saveexec_b64 s[6:7], vcc
	s_cbranch_execz .LBB0_290
.LBB0_314:
	s_waitcnt vmcnt(28)
	v_mov_b64_e32 v[74:75], v[166:167]
	v_mov_b64_e32 v[90:91], v[168:169]
	ds_read_b128 v[46:49], v161 offset:19456
	ds_read_b128 v[50:53], v161 offset:18432
	ds_read_b128 v[54:57], v161 offset:17408
	ds_read_b128 v[58:61], v161 offset:16384
	ds_read_b128 v[62:65], v161 offset:15360
	ds_read_b128 v[66:69], v161 offset:14336
	ds_read_b128 v[70:73], v161 offset:13312
	ds_read_b128 v[86:89], v161 offset:12288
	v_lshlrev_b32_e32 v92, 16, v74
	v_lshlrev_b32_e32 v45, 16, v90
	v_and_b32_e32 v93, 0xffff0000, v74
	v_and_b32_e32 v74, 0xffff0000, v90
	v_lshlrev_b32_e32 v81, 16, v91
	v_and_b32_e32 v90, 0xffff0000, v91
	v_mul_f32_e32 v45, 0xbfb8aa3b, v45
	v_mul_f32_e32 v74, 0xbfb8aa3b, v74
	v_mul_f32_e32 v81, 0xbfb8aa3b, v81
	v_mul_f32_e32 v90, 0xbfb8aa3b, v90
	v_exp_f32_e32 v45, v45
	v_exp_f32_e32 v74, v74
	v_exp_f32_e32 v81, v81
	v_exp_f32_e32 v90, v90
	v_add_f32_e32 v45, 1.0, v45
	v_add_f32_e32 v74, 1.0, v74
	v_add_f32_e32 v81, 1.0, v81
	v_add_f32_e32 v95, 1.0, v90
	v_rcp_f32_e32 v90, v45
	v_rcp_f32_e32 v91, v74
	v_rcp_f32_e32 v94, v81
	v_rcp_f32_e32 v95, v95
	v_lshlrev_b32_e32 v74, 16, v75
	v_and_b32_e32 v75, 0xffff0000, v75
	v_pk_mul_f32 v[90:91], v[90:91], v[92:93]
	v_pk_mul_f32 v[74:75], v[94:95], v[74:75]
	s_waitcnt lgkmcnt(3)
	v_pk_fma_f32 v[82:83], v[90:91], v[62:63], v[82:83]
	v_pk_fma_f32 v[84:85], v[64:65], v[74:75], v[84:85]
	v_pk_fma_f32 v[42:43], v[48:49], v[74:75], v[42:43]
	v_pk_fma_f32 v[40:41], v[46:47], v[90:91], v[40:41]
	v_pk_fma_f32 v[38:39], v[52:53], v[74:75], v[38:39]
	v_pk_fma_f32 v[36:37], v[50:51], v[90:91], v[36:37]
	v_pk_fma_f32 v[34:35], v[56:57], v[74:75], v[34:35]
	v_pk_fma_f32 v[32:33], v[54:55], v[90:91], v[32:33]
	v_pk_fma_f32 v[22:23], v[60:61], v[74:75], v[22:23]
	v_pk_fma_f32 v[20:21], v[58:59], v[90:91], v[20:21]
	s_waitcnt lgkmcnt(2)
	v_pk_fma_f32 v[26:27], v[74:75], v[68:69], v[26:27]
	v_pk_fma_f32 v[24:25], v[90:91], v[66:67], v[24:25]
	s_waitcnt lgkmcnt(1)
	v_pk_fma_f32 v[18:19], v[74:75], v[72:73], v[18:19]
	v_pk_fma_f32 v[16:17], v[90:91], v[70:71], v[16:17]
	s_waitcnt lgkmcnt(0)
	v_pk_fma_f32 v[30:31], v[74:75], v[88:89], v[30:31]
	v_pk_fma_f32 v[28:29], v[90:91], v[86:87], v[28:29]
	s_or_b64 exec, exec, s[6:7]
	v_cmp_lt_u32_e32 vcc, 13, v44
	s_and_saveexec_b64 s[6:7], vcc
	s_cbranch_execz .LBB0_291
.LBB0_315:
	s_waitcnt vmcnt(26)
	v_mov_b64_e32 v[74:75], v[170:171]
	v_mov_b64_e32 v[90:91], v[172:173]
	ds_read_b128 v[46:49], v161 offset:20480
	ds_read_b128 v[50:53], v161 offset:19456
	ds_read_b128 v[54:57], v161 offset:18432
	ds_read_b128 v[58:61], v161 offset:17408
	ds_read_b128 v[62:65], v161 offset:16384
	ds_read_b128 v[66:69], v161 offset:15360
	ds_read_b128 v[70:73], v161 offset:14336
	ds_read_b128 v[86:89], v161 offset:13312
	v_lshlrev_b32_e32 v92, 16, v74
	v_lshlrev_b32_e32 v45, 16, v90
	v_and_b32_e32 v93, 0xffff0000, v74
	v_and_b32_e32 v74, 0xffff0000, v90
	v_lshlrev_b32_e32 v81, 16, v91
	v_and_b32_e32 v90, 0xffff0000, v91
	v_mul_f32_e32 v45, 0xbfb8aa3b, v45
	v_mul_f32_e32 v74, 0xbfb8aa3b, v74
	v_mul_f32_e32 v81, 0xbfb8aa3b, v81
	v_mul_f32_e32 v90, 0xbfb8aa3b, v90
	v_exp_f32_e32 v45, v45
	v_exp_f32_e32 v74, v74
	v_exp_f32_e32 v81, v81
	v_exp_f32_e32 v90, v90
	v_add_f32_e32 v45, 1.0, v45
	v_add_f32_e32 v74, 1.0, v74
	v_add_f32_e32 v81, 1.0, v81
	v_add_f32_e32 v95, 1.0, v90
	v_rcp_f32_e32 v90, v45
	v_rcp_f32_e32 v91, v74
	v_rcp_f32_e32 v94, v81
	v_rcp_f32_e32 v95, v95
	v_lshlrev_b32_e32 v74, 16, v75
	v_and_b32_e32 v75, 0xffff0000, v75
	v_pk_mul_f32 v[90:91], v[90:91], v[92:93]
	v_pk_mul_f32 v[74:75], v[94:95], v[74:75]
	s_waitcnt lgkmcnt(3)
	v_pk_fma_f32 v[82:83], v[90:91], v[62:63], v[82:83]
	v_pk_fma_f32 v[84:85], v[64:65], v[74:75], v[84:85]
	v_pk_fma_f32 v[42:43], v[48:49], v[74:75], v[42:43]
	v_pk_fma_f32 v[40:41], v[46:47], v[90:91], v[40:41]
	v_pk_fma_f32 v[38:39], v[52:53], v[74:75], v[38:39]
	v_pk_fma_f32 v[36:37], v[50:51], v[90:91], v[36:37]
	v_pk_fma_f32 v[34:35], v[56:57], v[74:75], v[34:35]
	v_pk_fma_f32 v[32:33], v[54:55], v[90:91], v[32:33]
	v_pk_fma_f32 v[22:23], v[60:61], v[74:75], v[22:23]
	v_pk_fma_f32 v[20:21], v[58:59], v[90:91], v[20:21]
	s_waitcnt lgkmcnt(2)
	v_pk_fma_f32 v[26:27], v[74:75], v[68:69], v[26:27]
	v_pk_fma_f32 v[24:25], v[90:91], v[66:67], v[24:25]
	s_waitcnt lgkmcnt(1)
	v_pk_fma_f32 v[18:19], v[74:75], v[72:73], v[18:19]
	v_pk_fma_f32 v[16:17], v[90:91], v[70:71], v[16:17]
	s_waitcnt lgkmcnt(0)
	v_pk_fma_f32 v[30:31], v[74:75], v[88:89], v[30:31]
	v_pk_fma_f32 v[28:29], v[90:91], v[86:87], v[28:29]
	s_or_b64 exec, exec, s[6:7]
	v_cmp_lt_u32_e32 vcc, 12, v44
	s_and_saveexec_b64 s[6:7], vcc
	s_cbranch_execz .LBB0_292
.LBB0_316:
	s_waitcnt vmcnt(24)
	v_mov_b64_e32 v[74:75], v[176:177]
	v_mov_b64_e32 v[90:91], v[178:179]
	ds_read_b128 v[46:49], v161 offset:21504
	ds_read_b128 v[50:53], v161 offset:20480
	ds_read_b128 v[54:57], v161 offset:19456
	ds_read_b128 v[58:61], v161 offset:18432
	ds_read_b128 v[62:65], v161 offset:17408
	ds_read_b128 v[66:69], v161 offset:16384
	ds_read_b128 v[70:73], v161 offset:15360
	ds_read_b128 v[86:89], v161 offset:14336
	v_lshlrev_b32_e32 v92, 16, v74
	v_lshlrev_b32_e32 v45, 16, v90
	v_and_b32_e32 v93, 0xffff0000, v74
	v_and_b32_e32 v74, 0xffff0000, v90
	v_lshlrev_b32_e32 v81, 16, v91
	v_and_b32_e32 v90, 0xffff0000, v91
	v_mul_f32_e32 v45, 0xbfb8aa3b, v45
	v_mul_f32_e32 v74, 0xbfb8aa3b, v74
	v_mul_f32_e32 v81, 0xbfb8aa3b, v81
	v_mul_f32_e32 v90, 0xbfb8aa3b, v90
	v_exp_f32_e32 v45, v45
	v_exp_f32_e32 v74, v74
	v_exp_f32_e32 v81, v81
	v_exp_f32_e32 v90, v90
	v_add_f32_e32 v45, 1.0, v45
	v_add_f32_e32 v74, 1.0, v74
	v_add_f32_e32 v81, 1.0, v81
	v_add_f32_e32 v95, 1.0, v90
	v_rcp_f32_e32 v90, v45
	v_rcp_f32_e32 v91, v74
	v_rcp_f32_e32 v94, v81
	v_rcp_f32_e32 v95, v95
	v_lshlrev_b32_e32 v74, 16, v75
	v_and_b32_e32 v75, 0xffff0000, v75
	v_pk_mul_f32 v[90:91], v[90:91], v[92:93]
	v_pk_mul_f32 v[74:75], v[94:95], v[74:75]
	s_waitcnt lgkmcnt(3)
	v_pk_fma_f32 v[82:83], v[90:91], v[62:63], v[82:83]
	v_pk_fma_f32 v[84:85], v[64:65], v[74:75], v[84:85]
	v_pk_fma_f32 v[42:43], v[48:49], v[74:75], v[42:43]
	v_pk_fma_f32 v[40:41], v[46:47], v[90:91], v[40:41]
	v_pk_fma_f32 v[38:39], v[52:53], v[74:75], v[38:39]
	v_pk_fma_f32 v[36:37], v[50:51], v[90:91], v[36:37]
	v_pk_fma_f32 v[34:35], v[56:57], v[74:75], v[34:35]
	v_pk_fma_f32 v[32:33], v[54:55], v[90:91], v[32:33]
	v_pk_fma_f32 v[22:23], v[60:61], v[74:75], v[22:23]
	v_pk_fma_f32 v[20:21], v[58:59], v[90:91], v[20:21]
	s_waitcnt lgkmcnt(2)
	v_pk_fma_f32 v[26:27], v[74:75], v[68:69], v[26:27]
	v_pk_fma_f32 v[24:25], v[90:91], v[66:67], v[24:25]
	s_waitcnt lgkmcnt(1)
	v_pk_fma_f32 v[18:19], v[74:75], v[72:73], v[18:19]
	v_pk_fma_f32 v[16:17], v[90:91], v[70:71], v[16:17]
	s_waitcnt lgkmcnt(0)
	v_pk_fma_f32 v[30:31], v[74:75], v[88:89], v[30:31]
	v_pk_fma_f32 v[28:29], v[90:91], v[86:87], v[28:29]
	s_or_b64 exec, exec, s[6:7]
	v_cmp_lt_u32_e32 vcc, 11, v44
	s_and_saveexec_b64 s[6:7], vcc
	s_cbranch_execz .LBB0_293
.LBB0_317:
	s_waitcnt vmcnt(22)
	v_mov_b64_e32 v[74:75], v[180:181]
	v_mov_b64_e32 v[90:91], v[182:183]
	ds_read_b128 v[46:49], v161 offset:22528
	ds_read_b128 v[50:53], v161 offset:21504
	ds_read_b128 v[54:57], v161 offset:20480
	ds_read_b128 v[58:61], v161 offset:19456
	ds_read_b128 v[62:65], v161 offset:18432
	ds_read_b128 v[66:69], v161 offset:17408
	ds_read_b128 v[70:73], v161 offset:16384
	ds_read_b128 v[86:89], v161 offset:15360
	v_lshlrev_b32_e32 v92, 16, v74
	v_lshlrev_b32_e32 v45, 16, v90
	v_and_b32_e32 v93, 0xffff0000, v74
	v_and_b32_e32 v74, 0xffff0000, v90
	v_lshlrev_b32_e32 v81, 16, v91
	v_and_b32_e32 v90, 0xffff0000, v91
	v_mul_f32_e32 v45, 0xbfb8aa3b, v45
	v_mul_f32_e32 v74, 0xbfb8aa3b, v74
	v_mul_f32_e32 v81, 0xbfb8aa3b, v81
	v_mul_f32_e32 v90, 0xbfb8aa3b, v90
	v_exp_f32_e32 v45, v45
	v_exp_f32_e32 v74, v74
	v_exp_f32_e32 v81, v81
	v_exp_f32_e32 v90, v90
	v_add_f32_e32 v45, 1.0, v45
	v_add_f32_e32 v74, 1.0, v74
	v_add_f32_e32 v81, 1.0, v81
	v_add_f32_e32 v95, 1.0, v90
	v_rcp_f32_e32 v90, v45
	v_rcp_f32_e32 v91, v74
	v_rcp_f32_e32 v94, v81
	v_rcp_f32_e32 v95, v95
	v_lshlrev_b32_e32 v74, 16, v75
	v_and_b32_e32 v75, 0xffff0000, v75
	v_pk_mul_f32 v[90:91], v[90:91], v[92:93]
	v_pk_mul_f32 v[74:75], v[94:95], v[74:75]
	s_waitcnt lgkmcnt(3)
	v_pk_fma_f32 v[82:83], v[90:91], v[62:63], v[82:83]
	v_pk_fma_f32 v[84:85], v[64:65], v[74:75], v[84:85]
	v_pk_fma_f32 v[42:43], v[48:49], v[74:75], v[42:43]
	v_pk_fma_f32 v[40:41], v[46:47], v[90:91], v[40:41]
	v_pk_fma_f32 v[38:39], v[52:53], v[74:75], v[38:39]
	v_pk_fma_f32 v[36:37], v[50:51], v[90:91], v[36:37]
	v_pk_fma_f32 v[34:35], v[56:57], v[74:75], v[34:35]
	v_pk_fma_f32 v[32:33], v[54:55], v[90:91], v[32:33]
	v_pk_fma_f32 v[22:23], v[60:61], v[74:75], v[22:23]
	v_pk_fma_f32 v[20:21], v[58:59], v[90:91], v[20:21]
	s_waitcnt lgkmcnt(2)
	v_pk_fma_f32 v[26:27], v[74:75], v[68:69], v[26:27]
	v_pk_fma_f32 v[24:25], v[90:91], v[66:67], v[24:25]
	s_waitcnt lgkmcnt(1)
	v_pk_fma_f32 v[18:19], v[74:75], v[72:73], v[18:19]
	v_pk_fma_f32 v[16:17], v[90:91], v[70:71], v[16:17]
	s_waitcnt lgkmcnt(0)
	v_pk_fma_f32 v[30:31], v[74:75], v[88:89], v[30:31]
	v_pk_fma_f32 v[28:29], v[90:91], v[86:87], v[28:29]
	s_or_b64 exec, exec, s[6:7]
	v_cmp_lt_u32_e32 vcc, 10, v44
	s_and_saveexec_b64 s[6:7], vcc
	s_cbranch_execz .LBB0_294
.LBB0_318:
	s_waitcnt vmcnt(20)
	v_mov_b64_e32 v[74:75], v[186:187]
	v_mov_b64_e32 v[90:91], v[188:189]
	ds_read_b128 v[46:49], v161 offset:23552
	ds_read_b128 v[50:53], v161 offset:22528
	ds_read_b128 v[54:57], v161 offset:21504
	ds_read_b128 v[58:61], v161 offset:20480
	ds_read_b128 v[62:65], v161 offset:19456
	ds_read_b128 v[66:69], v161 offset:18432
	ds_read_b128 v[70:73], v161 offset:17408
	ds_read_b128 v[86:89], v161 offset:16384
	v_lshlrev_b32_e32 v92, 16, v74
	v_lshlrev_b32_e32 v45, 16, v90
	v_and_b32_e32 v93, 0xffff0000, v74
	v_and_b32_e32 v74, 0xffff0000, v90
	v_lshlrev_b32_e32 v81, 16, v91
	v_and_b32_e32 v90, 0xffff0000, v91
	v_mul_f32_e32 v45, 0xbfb8aa3b, v45
	v_mul_f32_e32 v74, 0xbfb8aa3b, v74
	v_mul_f32_e32 v81, 0xbfb8aa3b, v81
	v_mul_f32_e32 v90, 0xbfb8aa3b, v90
	v_exp_f32_e32 v45, v45
	v_exp_f32_e32 v74, v74
	v_exp_f32_e32 v81, v81
	v_exp_f32_e32 v90, v90
	v_add_f32_e32 v45, 1.0, v45
	v_add_f32_e32 v74, 1.0, v74
	v_add_f32_e32 v81, 1.0, v81
	v_add_f32_e32 v95, 1.0, v90
	v_rcp_f32_e32 v90, v45
	v_rcp_f32_e32 v91, v74
	v_rcp_f32_e32 v94, v81
	v_rcp_f32_e32 v95, v95
	v_lshlrev_b32_e32 v74, 16, v75
	v_and_b32_e32 v75, 0xffff0000, v75
	v_pk_mul_f32 v[90:91], v[90:91], v[92:93]
	v_pk_mul_f32 v[74:75], v[94:95], v[74:75]
	s_waitcnt lgkmcnt(3)
	v_pk_fma_f32 v[82:83], v[90:91], v[62:63], v[82:83]
	v_pk_fma_f32 v[84:85], v[64:65], v[74:75], v[84:85]
	v_pk_fma_f32 v[42:43], v[48:49], v[74:75], v[42:43]
	v_pk_fma_f32 v[40:41], v[46:47], v[90:91], v[40:41]
	v_pk_fma_f32 v[38:39], v[52:53], v[74:75], v[38:39]
	v_pk_fma_f32 v[36:37], v[50:51], v[90:91], v[36:37]
	v_pk_fma_f32 v[34:35], v[56:57], v[74:75], v[34:35]
	v_pk_fma_f32 v[32:33], v[54:55], v[90:91], v[32:33]
	v_pk_fma_f32 v[22:23], v[60:61], v[74:75], v[22:23]
	v_pk_fma_f32 v[20:21], v[58:59], v[90:91], v[20:21]
	s_waitcnt lgkmcnt(2)
	v_pk_fma_f32 v[26:27], v[74:75], v[68:69], v[26:27]
	v_pk_fma_f32 v[24:25], v[90:91], v[66:67], v[24:25]
	s_waitcnt lgkmcnt(1)
	v_pk_fma_f32 v[18:19], v[74:75], v[72:73], v[18:19]
	v_pk_fma_f32 v[16:17], v[90:91], v[70:71], v[16:17]
	s_waitcnt lgkmcnt(0)
	v_pk_fma_f32 v[30:31], v[74:75], v[88:89], v[30:31]
	v_pk_fma_f32 v[28:29], v[90:91], v[86:87], v[28:29]
	s_or_b64 exec, exec, s[6:7]
	v_cmp_lt_u32_e32 vcc, 9, v44
	s_and_saveexec_b64 s[6:7], vcc
	s_cbranch_execz .LBB0_295
.LBB0_319:
	s_waitcnt vmcnt(18)
	v_mov_b64_e32 v[74:75], v[206:207]
	v_mov_b64_e32 v[90:91], v[208:209]
	ds_read_b128 v[46:49], v161 offset:24576
	ds_read_b128 v[50:53], v161 offset:23552
	ds_read_b128 v[54:57], v161 offset:22528
	ds_read_b128 v[58:61], v161 offset:21504
	ds_read_b128 v[62:65], v161 offset:20480
	ds_read_b128 v[66:69], v161 offset:19456
	ds_read_b128 v[70:73], v161 offset:18432
	ds_read_b128 v[86:89], v161 offset:17408
	v_lshlrev_b32_e32 v92, 16, v74
	v_lshlrev_b32_e32 v45, 16, v90
	v_and_b32_e32 v93, 0xffff0000, v74
	v_and_b32_e32 v74, 0xffff0000, v90
	v_lshlrev_b32_e32 v81, 16, v91
	v_and_b32_e32 v90, 0xffff0000, v91
	v_mul_f32_e32 v45, 0xbfb8aa3b, v45
	v_mul_f32_e32 v74, 0xbfb8aa3b, v74
	v_mul_f32_e32 v81, 0xbfb8aa3b, v81
	v_mul_f32_e32 v90, 0xbfb8aa3b, v90
	v_exp_f32_e32 v45, v45
	v_exp_f32_e32 v74, v74
	v_exp_f32_e32 v81, v81
	v_exp_f32_e32 v90, v90
	v_add_f32_e32 v45, 1.0, v45
	v_add_f32_e32 v74, 1.0, v74
	v_add_f32_e32 v81, 1.0, v81
	v_add_f32_e32 v95, 1.0, v90
	v_rcp_f32_e32 v90, v45
	v_rcp_f32_e32 v91, v74
	v_rcp_f32_e32 v94, v81
	v_rcp_f32_e32 v95, v95
	v_lshlrev_b32_e32 v74, 16, v75
	v_and_b32_e32 v75, 0xffff0000, v75
	v_pk_mul_f32 v[90:91], v[90:91], v[92:93]
	v_pk_mul_f32 v[74:75], v[94:95], v[74:75]
	s_waitcnt lgkmcnt(3)
	v_pk_fma_f32 v[82:83], v[90:91], v[62:63], v[82:83]
	v_pk_fma_f32 v[84:85], v[64:65], v[74:75], v[84:85]
	v_pk_fma_f32 v[42:43], v[48:49], v[74:75], v[42:43]
	v_pk_fma_f32 v[40:41], v[46:47], v[90:91], v[40:41]
	v_pk_fma_f32 v[38:39], v[52:53], v[74:75], v[38:39]
	v_pk_fma_f32 v[36:37], v[50:51], v[90:91], v[36:37]
	v_pk_fma_f32 v[34:35], v[56:57], v[74:75], v[34:35]
	v_pk_fma_f32 v[32:33], v[54:55], v[90:91], v[32:33]
	v_pk_fma_f32 v[22:23], v[60:61], v[74:75], v[22:23]
	v_pk_fma_f32 v[20:21], v[58:59], v[90:91], v[20:21]
	s_waitcnt lgkmcnt(2)
	v_pk_fma_f32 v[26:27], v[74:75], v[68:69], v[26:27]
	v_pk_fma_f32 v[24:25], v[90:91], v[66:67], v[24:25]
	s_waitcnt lgkmcnt(1)
	v_pk_fma_f32 v[18:19], v[74:75], v[72:73], v[18:19]
	v_pk_fma_f32 v[16:17], v[90:91], v[70:71], v[16:17]
	s_waitcnt lgkmcnt(0)
	v_pk_fma_f32 v[30:31], v[74:75], v[88:89], v[30:31]
	v_pk_fma_f32 v[28:29], v[90:91], v[86:87], v[28:29]
	s_or_b64 exec, exec, s[6:7]
	v_cmp_lt_u32_e32 vcc, 8, v44
	s_and_saveexec_b64 s[6:7], vcc
	s_cbranch_execz .LBB0_296
.LBB0_320:
	s_waitcnt vmcnt(16)
	v_mov_b64_e32 v[74:75], v[210:211]
	v_mov_b64_e32 v[90:91], v[212:213]
	ds_read_b128 v[46:49], v161 offset:25600
	ds_read_b128 v[50:53], v161 offset:24576
	ds_read_b128 v[54:57], v161 offset:23552
	ds_read_b128 v[58:61], v161 offset:22528
	ds_read_b128 v[62:65], v161 offset:21504
	ds_read_b128 v[66:69], v161 offset:20480
	ds_read_b128 v[70:73], v161 offset:19456
	ds_read_b128 v[86:89], v161 offset:18432
	v_lshlrev_b32_e32 v92, 16, v74
	v_lshlrev_b32_e32 v45, 16, v90
	v_and_b32_e32 v93, 0xffff0000, v74
	v_and_b32_e32 v74, 0xffff0000, v90
	v_lshlrev_b32_e32 v81, 16, v91
	v_and_b32_e32 v90, 0xffff0000, v91
	v_mul_f32_e32 v45, 0xbfb8aa3b, v45
	v_mul_f32_e32 v74, 0xbfb8aa3b, v74
	v_mul_f32_e32 v81, 0xbfb8aa3b, v81
	v_mul_f32_e32 v90, 0xbfb8aa3b, v90
	v_exp_f32_e32 v45, v45
	v_exp_f32_e32 v74, v74
	v_exp_f32_e32 v81, v81
	v_exp_f32_e32 v90, v90
	v_add_f32_e32 v45, 1.0, v45
	v_add_f32_e32 v74, 1.0, v74
	v_add_f32_e32 v81, 1.0, v81
	v_add_f32_e32 v95, 1.0, v90
	v_rcp_f32_e32 v90, v45
	v_rcp_f32_e32 v91, v74
	v_rcp_f32_e32 v94, v81
	v_rcp_f32_e32 v95, v95
	v_lshlrev_b32_e32 v74, 16, v75
	v_and_b32_e32 v75, 0xffff0000, v75
	v_pk_mul_f32 v[90:91], v[90:91], v[92:93]
	v_pk_mul_f32 v[74:75], v[94:95], v[74:75]
	s_waitcnt lgkmcnt(3)
	v_pk_fma_f32 v[82:83], v[90:91], v[62:63], v[82:83]
	v_pk_fma_f32 v[84:85], v[64:65], v[74:75], v[84:85]
	v_pk_fma_f32 v[42:43], v[48:49], v[74:75], v[42:43]
	v_pk_fma_f32 v[40:41], v[46:47], v[90:91], v[40:41]
	v_pk_fma_f32 v[38:39], v[52:53], v[74:75], v[38:39]
	v_pk_fma_f32 v[36:37], v[50:51], v[90:91], v[36:37]
	v_pk_fma_f32 v[34:35], v[56:57], v[74:75], v[34:35]
	v_pk_fma_f32 v[32:33], v[54:55], v[90:91], v[32:33]
	v_pk_fma_f32 v[22:23], v[60:61], v[74:75], v[22:23]
	v_pk_fma_f32 v[20:21], v[58:59], v[90:91], v[20:21]
	s_waitcnt lgkmcnt(2)
	v_pk_fma_f32 v[26:27], v[74:75], v[68:69], v[26:27]
	v_pk_fma_f32 v[24:25], v[90:91], v[66:67], v[24:25]
	s_waitcnt lgkmcnt(1)
	v_pk_fma_f32 v[18:19], v[74:75], v[72:73], v[18:19]
	v_pk_fma_f32 v[16:17], v[90:91], v[70:71], v[16:17]
	s_waitcnt lgkmcnt(0)
	v_pk_fma_f32 v[30:31], v[74:75], v[88:89], v[30:31]
	v_pk_fma_f32 v[28:29], v[90:91], v[86:87], v[28:29]
	s_or_b64 exec, exec, s[6:7]
	v_cmp_ne_u32_e32 vcc, 0, v44
	s_and_saveexec_b64 s[6:7], vcc
	s_cbranch_execz .LBB0_297
.LBB0_321:
	s_waitcnt vmcnt(14)
	v_mov_b64_e32 v[86:87], v[214:215]
	v_mov_b64_e32 v[88:89], v[216:217]
	ds_read_b128 v[44:47], v161 offset:26624
	ds_read_b128 v[48:51], v161 offset:25600
	ds_read_b128 v[52:55], v161 offset:24576
	ds_read_b128 v[56:59], v161 offset:23552
	ds_read_b128 v[60:63], v161 offset:22528
	ds_read_b128 v[64:67], v161 offset:21504
	ds_read_b128 v[68:71], v161 offset:20480
	ds_read_b128 v[72:75], v161 offset:19456
	v_lshlrev_b32_e32 v90, 16, v86
	v_lshlrev_b32_e32 v81, 16, v88
	v_and_b32_e32 v91, 0xffff0000, v86
	v_and_b32_e32 v86, 0xffff0000, v88
	v_lshlrev_b32_e32 v88, 16, v89
	v_and_b32_e32 v89, 0xffff0000, v89
	v_mul_f32_e32 v81, 0xbfb8aa3b, v81
	v_mul_f32_e32 v86, 0xbfb8aa3b, v86
	v_mul_f32_e32 v88, 0xbfb8aa3b, v88
	v_mul_f32_e32 v89, 0xbfb8aa3b, v89
	v_exp_f32_e32 v81, v81
	v_exp_f32_e32 v86, v86
	v_exp_f32_e32 v88, v88
	v_exp_f32_e32 v89, v89
	v_add_f32_e32 v81, 1.0, v81
	v_add_f32_e32 v86, 1.0, v86
	v_add_f32_e32 v92, 1.0, v88
	v_add_f32_e32 v93, 1.0, v89
	v_rcp_f32_e32 v88, v81
	v_rcp_f32_e32 v89, v86
	v_rcp_f32_e32 v92, v92
	v_rcp_f32_e32 v93, v93
	v_lshlrev_b32_e32 v86, 16, v87
	v_and_b32_e32 v87, 0xffff0000, v87
	v_pk_mul_f32 v[88:89], v[88:89], v[90:91]
	v_pk_mul_f32 v[86:87], v[92:93], v[86:87]
	s_waitcnt lgkmcnt(3)
	v_pk_fma_f32 v[82:83], v[88:89], v[60:61], v[82:83]
	v_pk_fma_f32 v[84:85], v[62:63], v[86:87], v[84:85]
	v_pk_fma_f32 v[42:43], v[46:47], v[86:87], v[42:43]
	v_pk_fma_f32 v[40:41], v[44:45], v[88:89], v[40:41]
	v_pk_fma_f32 v[38:39], v[50:51], v[86:87], v[38:39]
	v_pk_fma_f32 v[36:37], v[48:49], v[88:89], v[36:37]
	v_pk_fma_f32 v[34:35], v[54:55], v[86:87], v[34:35]
	v_pk_fma_f32 v[32:33], v[52:53], v[88:89], v[32:33]
	v_pk_fma_f32 v[22:23], v[58:59], v[86:87], v[22:23]
	v_pk_fma_f32 v[20:21], v[56:57], v[88:89], v[20:21]
	s_waitcnt lgkmcnt(2)
	v_pk_fma_f32 v[26:27], v[86:87], v[66:67], v[26:27]
	v_pk_fma_f32 v[24:25], v[88:89], v[64:65], v[24:25]
	s_waitcnt lgkmcnt(1)
	v_pk_fma_f32 v[18:19], v[86:87], v[70:71], v[18:19]
	v_pk_fma_f32 v[16:17], v[88:89], v[68:69], v[16:17]
	s_waitcnt lgkmcnt(0)
	v_pk_fma_f32 v[30:31], v[86:87], v[74:75], v[30:31]
	v_pk_fma_f32 v[28:29], v[88:89], v[72:73], v[28:29]
	s_or_b64 exec, exec, s[6:7]
	ds_read_b128 v[44:47], v161 offset:27648
	s_and_saveexec_b64 s[6:7], vcc
	s_cbranch_execz .LBB0_298
.LBB0_322:
	s_waitcnt vmcnt(12)
	v_mov_b64_e32 v[86:87], v[218:219]
	v_mov_b64_e32 v[88:89], v[220:221]
	ds_read_b128 v[48:51], v161 offset:26624
	ds_read_b128 v[52:55], v161 offset:25600
	ds_read_b128 v[56:59], v161 offset:24576
	ds_read_b128 v[60:63], v161 offset:23552
	ds_read_b128 v[64:67], v161 offset:22528
	ds_read_b128 v[68:71], v161 offset:21504
	ds_read_b128 v[72:75], v161 offset:20480
	v_lshlrev_b32_e32 v90, 16, v86
	v_lshlrev_b32_e32 v81, 16, v88
	v_and_b32_e32 v91, 0xffff0000, v86
	v_and_b32_e32 v86, 0xffff0000, v88
	v_lshlrev_b32_e32 v88, 16, v89
	v_and_b32_e32 v89, 0xffff0000, v89
	v_mul_f32_e32 v81, 0xbfb8aa3b, v81
	v_mul_f32_e32 v86, 0xbfb8aa3b, v86
	v_mul_f32_e32 v88, 0xbfb8aa3b, v88
	v_mul_f32_e32 v89, 0xbfb8aa3b, v89
	v_exp_f32_e32 v81, v81
	v_exp_f32_e32 v86, v86
	v_exp_f32_e32 v88, v88
	v_exp_f32_e32 v89, v89
	v_add_f32_e32 v81, 1.0, v81
	v_add_f32_e32 v86, 1.0, v86
	v_add_f32_e32 v92, 1.0, v88
	v_add_f32_e32 v93, 1.0, v89
	v_rcp_f32_e32 v88, v81
	v_rcp_f32_e32 v89, v86
	v_rcp_f32_e32 v92, v92
	v_rcp_f32_e32 v93, v93
	v_lshlrev_b32_e32 v86, 16, v87
	v_and_b32_e32 v87, 0xffff0000, v87
	v_pk_mul_f32 v[88:89], v[88:89], v[90:91]
	v_pk_mul_f32 v[86:87], v[92:93], v[86:87]
	s_waitcnt lgkmcnt(3)
	v_pk_fma_f32 v[82:83], v[88:89], v[60:61], v[82:83]
	v_pk_fma_f32 v[84:85], v[62:63], v[86:87], v[84:85]
	v_pk_fma_f32 v[42:43], v[46:47], v[86:87], v[42:43]
	v_pk_fma_f32 v[40:41], v[44:45], v[88:89], v[40:41]
	v_pk_fma_f32 v[38:39], v[50:51], v[86:87], v[38:39]
	v_pk_fma_f32 v[36:37], v[48:49], v[88:89], v[36:37]
	v_pk_fma_f32 v[34:35], v[54:55], v[86:87], v[34:35]
	v_pk_fma_f32 v[32:33], v[52:53], v[88:89], v[32:33]
	v_pk_fma_f32 v[22:23], v[58:59], v[86:87], v[22:23]
	v_pk_fma_f32 v[20:21], v[56:57], v[88:89], v[20:21]
	s_waitcnt lgkmcnt(2)
	v_pk_fma_f32 v[26:27], v[86:87], v[66:67], v[26:27]
	v_pk_fma_f32 v[24:25], v[88:89], v[64:65], v[24:25]
	s_waitcnt lgkmcnt(1)
	v_pk_fma_f32 v[18:19], v[86:87], v[70:71], v[18:19]
	v_pk_fma_f32 v[16:17], v[88:89], v[68:69], v[16:17]
	s_waitcnt lgkmcnt(0)
	v_pk_fma_f32 v[30:31], v[86:87], v[74:75], v[30:31]
	v_pk_fma_f32 v[28:29], v[88:89], v[72:73], v[28:29]
	s_or_b64 exec, exec, s[6:7]
	ds_read_b128 v[48:51], v161 offset:28672
	s_and_saveexec_b64 s[6:7], vcc
	s_cbranch_execz .LBB0_299
.LBB0_323:
	s_waitcnt vmcnt(10)
	v_mov_b64_e32 v[86:87], v[222:223]
	v_mov_b64_e32 v[88:89], v[224:225]
	ds_read_b128 v[52:55], v161 offset:26624
	ds_read_b128 v[56:59], v161 offset:25600
	ds_read_b128 v[60:63], v161 offset:24576
	ds_read_b128 v[64:67], v161 offset:23552
	ds_read_b128 v[68:71], v161 offset:22528
	ds_read_b128 v[72:75], v161 offset:21504
	v_lshlrev_b32_e32 v90, 16, v86
	v_lshlrev_b32_e32 v81, 16, v88
	v_and_b32_e32 v91, 0xffff0000, v86
	v_and_b32_e32 v86, 0xffff0000, v88
	v_lshlrev_b32_e32 v88, 16, v89
	v_and_b32_e32 v89, 0xffff0000, v89
	v_mul_f32_e32 v81, 0xbfb8aa3b, v81
	v_mul_f32_e32 v86, 0xbfb8aa3b, v86
	v_mul_f32_e32 v88, 0xbfb8aa3b, v88
	v_mul_f32_e32 v89, 0xbfb8aa3b, v89
	v_exp_f32_e32 v81, v81
	v_exp_f32_e32 v86, v86
	v_exp_f32_e32 v88, v88
	v_exp_f32_e32 v89, v89
	v_add_f32_e32 v81, 1.0, v81
	v_add_f32_e32 v86, 1.0, v86
	v_add_f32_e32 v92, 1.0, v88
	v_add_f32_e32 v93, 1.0, v89
	v_rcp_f32_e32 v88, v81
	v_rcp_f32_e32 v89, v86
	v_rcp_f32_e32 v92, v92
	v_rcp_f32_e32 v93, v93
	v_lshlrev_b32_e32 v86, 16, v87
	v_and_b32_e32 v87, 0xffff0000, v87
	v_pk_mul_f32 v[88:89], v[88:89], v[90:91]
	v_pk_mul_f32 v[86:87], v[92:93], v[86:87]
	s_waitcnt lgkmcnt(3)
	v_pk_fma_f32 v[82:83], v[88:89], v[60:61], v[82:83]
	v_pk_fma_f32 v[84:85], v[62:63], v[86:87], v[84:85]
	v_pk_fma_f32 v[42:43], v[50:51], v[86:87], v[42:43]
	v_pk_fma_f32 v[40:41], v[48:49], v[88:89], v[40:41]
	v_pk_fma_f32 v[38:39], v[46:47], v[86:87], v[38:39]
	v_pk_fma_f32 v[36:37], v[44:45], v[88:89], v[36:37]
	v_pk_fma_f32 v[34:35], v[54:55], v[86:87], v[34:35]
	v_pk_fma_f32 v[32:33], v[52:53], v[88:89], v[32:33]
	v_pk_fma_f32 v[22:23], v[58:59], v[86:87], v[22:23]
	v_pk_fma_f32 v[20:21], v[56:57], v[88:89], v[20:21]
	s_waitcnt lgkmcnt(2)
	v_pk_fma_f32 v[26:27], v[86:87], v[66:67], v[26:27]
	v_pk_fma_f32 v[24:25], v[88:89], v[64:65], v[24:25]
	s_waitcnt lgkmcnt(1)
	v_pk_fma_f32 v[18:19], v[86:87], v[70:71], v[18:19]
	v_pk_fma_f32 v[16:17], v[88:89], v[68:69], v[16:17]
	s_waitcnt lgkmcnt(0)
	v_pk_fma_f32 v[30:31], v[86:87], v[74:75], v[30:31]
	v_pk_fma_f32 v[28:29], v[88:89], v[72:73], v[28:29]
	s_or_b64 exec, exec, s[6:7]
	ds_read_b128 v[52:55], v161 offset:29696
	s_and_saveexec_b64 s[6:7], vcc
	s_cbranch_execz .LBB0_300
.LBB0_324:
	s_waitcnt vmcnt(8)
	v_mov_b64_e32 v[86:87], v[226:227]
	v_mov_b64_e32 v[88:89], v[228:229]
	ds_read_b128 v[56:59], v161 offset:26624
	ds_read_b128 v[60:63], v161 offset:25600
	ds_read_b128 v[64:67], v161 offset:24576
	ds_read_b128 v[68:71], v161 offset:23552
	ds_read_b128 v[72:75], v161 offset:22528
	v_lshlrev_b32_e32 v90, 16, v86
	v_lshlrev_b32_e32 v81, 16, v88
	v_and_b32_e32 v91, 0xffff0000, v86
	v_and_b32_e32 v86, 0xffff0000, v88
	v_lshlrev_b32_e32 v88, 16, v89
	v_and_b32_e32 v89, 0xffff0000, v89
	v_mul_f32_e32 v81, 0xbfb8aa3b, v81
	v_mul_f32_e32 v86, 0xbfb8aa3b, v86
	v_mul_f32_e32 v88, 0xbfb8aa3b, v88
	v_mul_f32_e32 v89, 0xbfb8aa3b, v89
	v_exp_f32_e32 v81, v81
	v_exp_f32_e32 v86, v86
	v_exp_f32_e32 v88, v88
	v_exp_f32_e32 v89, v89
	v_add_f32_e32 v81, 1.0, v81
	v_add_f32_e32 v86, 1.0, v86
	v_add_f32_e32 v92, 1.0, v88
	v_add_f32_e32 v93, 1.0, v89
	v_rcp_f32_e32 v88, v81
	v_rcp_f32_e32 v89, v86
	v_rcp_f32_e32 v92, v92
	v_rcp_f32_e32 v93, v93
	v_lshlrev_b32_e32 v86, 16, v87
	v_and_b32_e32 v87, 0xffff0000, v87
	v_pk_mul_f32 v[88:89], v[88:89], v[90:91]
	v_pk_mul_f32 v[86:87], v[92:93], v[86:87]
	s_waitcnt lgkmcnt(3)
	v_pk_fma_f32 v[82:83], v[88:89], v[60:61], v[82:83]
	v_pk_fma_f32 v[84:85], v[62:63], v[86:87], v[84:85]
	v_pk_fma_f32 v[42:43], v[54:55], v[86:87], v[42:43]
	v_pk_fma_f32 v[40:41], v[52:53], v[88:89], v[40:41]
	v_pk_fma_f32 v[38:39], v[50:51], v[86:87], v[38:39]
	v_pk_fma_f32 v[36:37], v[48:49], v[88:89], v[36:37]
	v_pk_fma_f32 v[34:35], v[46:47], v[86:87], v[34:35]
	v_pk_fma_f32 v[32:33], v[44:45], v[88:89], v[32:33]
	v_pk_fma_f32 v[22:23], v[58:59], v[86:87], v[22:23]
	v_pk_fma_f32 v[20:21], v[56:57], v[88:89], v[20:21]
	s_waitcnt lgkmcnt(2)
	v_pk_fma_f32 v[26:27], v[86:87], v[66:67], v[26:27]
	v_pk_fma_f32 v[24:25], v[88:89], v[64:65], v[24:25]
	s_waitcnt lgkmcnt(1)
	v_pk_fma_f32 v[18:19], v[86:87], v[70:71], v[18:19]
	v_pk_fma_f32 v[16:17], v[88:89], v[68:69], v[16:17]
	s_waitcnt lgkmcnt(0)
	v_pk_fma_f32 v[30:31], v[86:87], v[74:75], v[30:31]
	v_pk_fma_f32 v[28:29], v[88:89], v[72:73], v[28:29]
	s_or_b64 exec, exec, s[6:7]
	ds_read_b128 v[56:59], v161 offset:30720
	s_and_saveexec_b64 s[6:7], vcc
	s_cbranch_execz .LBB0_301
.LBB0_325:
	s_waitcnt vmcnt(6)
	v_mov_b64_e32 v[86:87], v[230:231]
	v_mov_b64_e32 v[88:89], v[232:233]
	ds_read_b128 v[60:63], v161 offset:26624
	ds_read_b128 v[64:67], v161 offset:25600
	ds_read_b128 v[68:71], v161 offset:24576
	ds_read_b128 v[72:75], v161 offset:23552
	v_lshlrev_b32_e32 v90, 16, v86
	v_lshlrev_b32_e32 v81, 16, v88
	v_and_b32_e32 v91, 0xffff0000, v86
	v_and_b32_e32 v86, 0xffff0000, v88
	v_lshlrev_b32_e32 v88, 16, v89
	v_and_b32_e32 v89, 0xffff0000, v89
	v_mul_f32_e32 v81, 0xbfb8aa3b, v81
	v_mul_f32_e32 v86, 0xbfb8aa3b, v86
	v_mul_f32_e32 v88, 0xbfb8aa3b, v88
	v_mul_f32_e32 v89, 0xbfb8aa3b, v89
	v_exp_f32_e32 v81, v81
	v_exp_f32_e32 v86, v86
	v_exp_f32_e32 v88, v88
	v_exp_f32_e32 v89, v89
	v_add_f32_e32 v81, 1.0, v81
	v_add_f32_e32 v86, 1.0, v86
	v_add_f32_e32 v92, 1.0, v88
	v_add_f32_e32 v93, 1.0, v89
	v_rcp_f32_e32 v88, v81
	v_rcp_f32_e32 v89, v86
	v_rcp_f32_e32 v92, v92
	v_rcp_f32_e32 v93, v93
	v_lshlrev_b32_e32 v86, 16, v87
	v_and_b32_e32 v87, 0xffff0000, v87
	v_pk_mul_f32 v[88:89], v[88:89], v[90:91]
	v_pk_mul_f32 v[86:87], v[92:93], v[86:87]
	s_waitcnt lgkmcnt(3)
	v_pk_fma_f32 v[82:83], v[88:89], v[60:61], v[82:83]
	v_pk_fma_f32 v[84:85], v[62:63], v[86:87], v[84:85]
	v_pk_fma_f32 v[42:43], v[58:59], v[86:87], v[42:43]
	v_pk_fma_f32 v[40:41], v[56:57], v[88:89], v[40:41]
	v_pk_fma_f32 v[38:39], v[54:55], v[86:87], v[38:39]
	v_pk_fma_f32 v[36:37], v[52:53], v[88:89], v[36:37]
	v_pk_fma_f32 v[34:35], v[50:51], v[86:87], v[34:35]
	v_pk_fma_f32 v[32:33], v[48:49], v[88:89], v[32:33]
	v_pk_fma_f32 v[22:23], v[46:47], v[86:87], v[22:23]
	v_pk_fma_f32 v[20:21], v[44:45], v[88:89], v[20:21]
	s_waitcnt lgkmcnt(2)
	v_pk_fma_f32 v[26:27], v[86:87], v[66:67], v[26:27]
	v_pk_fma_f32 v[24:25], v[88:89], v[64:65], v[24:25]
	s_waitcnt lgkmcnt(1)
	v_pk_fma_f32 v[18:19], v[86:87], v[70:71], v[18:19]
	v_pk_fma_f32 v[16:17], v[88:89], v[68:69], v[16:17]
	s_waitcnt lgkmcnt(0)
	v_pk_fma_f32 v[30:31], v[86:87], v[74:75], v[30:31]
	v_pk_fma_f32 v[28:29], v[88:89], v[72:73], v[28:29]
	s_or_b64 exec, exec, s[6:7]
	ds_read_b128 v[60:63], v161 offset:31744
	s_and_saveexec_b64 s[6:7], vcc
	s_cbranch_execz .LBB0_302
.LBB0_326:
	s_waitcnt vmcnt(4)
	v_mov_b64_e32 v[86:87], v[234:235]
	v_mov_b64_e32 v[88:89], v[236:237]
	ds_read_b128 v[64:67], v161 offset:26624
	ds_read_b128 v[68:71], v161 offset:25600
	ds_read_b128 v[72:75], v161 offset:24576
	v_lshlrev_b32_e32 v90, 16, v86
	v_lshlrev_b32_e32 v81, 16, v88
	v_and_b32_e32 v91, 0xffff0000, v86
	v_and_b32_e32 v86, 0xffff0000, v88
	v_lshlrev_b32_e32 v88, 16, v89
	v_and_b32_e32 v89, 0xffff0000, v89
	v_mul_f32_e32 v81, 0xbfb8aa3b, v81
	v_mul_f32_e32 v86, 0xbfb8aa3b, v86
	v_mul_f32_e32 v88, 0xbfb8aa3b, v88
	v_mul_f32_e32 v89, 0xbfb8aa3b, v89
	v_exp_f32_e32 v81, v81
	v_exp_f32_e32 v86, v86
	v_exp_f32_e32 v88, v88
	v_exp_f32_e32 v89, v89
	v_add_f32_e32 v81, 1.0, v81
	v_add_f32_e32 v86, 1.0, v86
	v_add_f32_e32 v92, 1.0, v88
	v_add_f32_e32 v93, 1.0, v89
	v_rcp_f32_e32 v88, v81
	v_rcp_f32_e32 v89, v86
	v_rcp_f32_e32 v92, v92
	v_rcp_f32_e32 v93, v93
	v_lshlrev_b32_e32 v86, 16, v87
	v_and_b32_e32 v87, 0xffff0000, v87
	v_pk_mul_f32 v[88:89], v[88:89], v[90:91]
	v_pk_mul_f32 v[86:87], v[92:93], v[86:87]
	s_waitcnt lgkmcnt(7)
	v_pk_fma_f32 v[82:83], v[88:89], v[44:45], v[82:83]
	v_pk_fma_f32 v[84:85], v[46:47], v[86:87], v[84:85]
	s_waitcnt lgkmcnt(3)
	v_pk_fma_f32 v[42:43], v[62:63], v[86:87], v[42:43]
	v_pk_fma_f32 v[40:41], v[60:61], v[88:89], v[40:41]
	v_pk_fma_f32 v[38:39], v[58:59], v[86:87], v[38:39]
	v_pk_fma_f32 v[36:37], v[56:57], v[88:89], v[36:37]
	v_pk_fma_f32 v[34:35], v[54:55], v[86:87], v[34:35]
	v_pk_fma_f32 v[32:33], v[52:53], v[88:89], v[32:33]
	v_pk_fma_f32 v[22:23], v[50:51], v[86:87], v[22:23]
	v_pk_fma_f32 v[20:21], v[48:49], v[88:89], v[20:21]
	s_waitcnt lgkmcnt(2)
	v_pk_fma_f32 v[26:27], v[86:87], v[66:67], v[26:27]
	v_pk_fma_f32 v[24:25], v[88:89], v[64:65], v[24:25]
	s_waitcnt lgkmcnt(1)
	v_pk_fma_f32 v[18:19], v[86:87], v[70:71], v[18:19]
	v_pk_fma_f32 v[16:17], v[88:89], v[68:69], v[16:17]
	s_waitcnt lgkmcnt(0)
	v_pk_fma_f32 v[30:31], v[86:87], v[74:75], v[30:31]
	v_pk_fma_f32 v[28:29], v[88:89], v[72:73], v[28:29]
	s_or_b64 exec, exec, s[6:7]
	ds_read_b128 v[64:67], v161 offset:32768
	s_and_saveexec_b64 s[6:7], vcc
	s_cbranch_execnz .LBB0_303
	s_branch .LBB0_304
